# speedup vs baseline: 1.0060x; 1.0020x over previous
.LBB4_12:
	s_add_u32 s81, s40, s22
	s_addc_u32 s82, s41, s23
	s_add_u32 s29, s40, 0x100
	s_addc_u32 s44, s41, 0
	s_and_b64 s[42:43], s[14:15], exec
	ds_read_b128 v[82:85], v161
	ds_read_b128 v[94:97], v161 offset:2048
	ds_read_b128 v[102:105], v162
	ds_read_b128 v[110:113], v162 offset:2048
	s_cselect_b32 s47, s37, s44
	s_cselect_b32 s46, s36, s29
	s_add_u32 s29, s38, 0x100
	s_addc_u32 s44, s39, 0
	s_and_b64 s[42:43], s[14:15], exec
	s_cselect_b32 s49, s5, s44
	s_cselect_b32 s48, s4, s29
	s_add_u32 s44, s46, 0x80
	s_addc_u32 s45, s47, 0
	s_add_u32 s42, s48, 0x80
	s_addc_u32 s43, s49, 0
	ds_read_b128 v[58:61], v163
	ds_read_b128 v[66:69], v163 offset:2048
	ds_read_b128 v[62:65], v164
	ds_read_b128 v[70:73], v164 offset:2048
	ds_read_b128 v[74:77], v163 offset:4096
	ds_read_b128 v[86:89], v163 offset:6144
	ds_read_b128 v[78:81], v164 offset:4096
	ds_read_b128 v[90:93], v164 offset:6144
	s_add_u32 s78, s81, 0x80
	s_addc_u32 s79, s82, 0
	s_mov_b32 m0, s70
	s_nop 0
	global_load_lds_dwordx4 v146, s[78:79]
	s_mov_b32 m0, s71
	s_nop 0
	global_load_lds_dwordx4 v150, s[78:79]
	s_waitcnt lgkmcnt(8)
	s_barrier
	s_waitcnt lgkmcnt(0)
	s_waitcnt vmcnt(16)
	v_mov_b32_e32 v1, v0
	v_pk_mul_f32 v[16:17], v[0:1], v[16:17]
	v_pk_mul_f32 v[14:15], v[154:155], v[14:15]
	v_pk_mul_f32 v[12:13], v[0:1], v[12:13]
	v_pk_mul_f32 v[10:11], v[154:155], v[10:11]
	v_pk_mul_f32 v[8:9], v[0:1], v[8:9]
	v_pk_mul_f32 v[6:7], v[154:155], v[6:7]
	v_pk_mul_f32 v[4:5], v[0:1], v[4:5]
	v_pk_mul_f32 v[2:3], v[154:155], v[2:3]
	s_setprio 1
	v_mfma_f32_16x16x128_f8f6f4 v[18:21], v[82:85], v[58:61], v[14:17] cbsz:4 blgp:4
	v_mfma_f32_16x16x128_f8f6f4 v[22:25], v[94:97], v[58:61], v[10:13] cbsz:4 blgp:4
	v_mfma_f32_16x16x128_f8f6f4 v[26:29], v[82:85], v[66:69], v[14:17] cbsz:4 blgp:4
	v_mfma_f32_16x16x128_f8f6f4 v[30:33], v[94:97], v[66:69], v[10:13] cbsz:4 blgp:4
	v_mfma_f32_16x16x128_f8f6f4 v[34:37], v[82:85], v[74:77], v[14:17] cbsz:4 blgp:4
	v_mfma_f32_16x16x128_f8f6f4 v[38:41], v[94:97], v[74:77], v[10:13] cbsz:4 blgp:4
	v_mfma_f32_16x16x128_f8f6f4 v[42:45], v[82:85], v[86:89], v[14:17] cbsz:4 blgp:4
	v_mfma_f32_16x16x128_f8f6f4 v[46:49], v[94:97], v[86:89], v[10:13] cbsz:4 blgp:4
	v_mfma_f32_16x16x128_f8f6f4 v[18:21], v[102:105], v[62:65], v[18:21] cbsz:4 blgp:4
	v_mfma_f32_16x16x128_f8f6f4 v[22:25], v[110:113], v[62:65], v[22:25] cbsz:4 blgp:4
	v_mfma_f32_16x16x128_f8f6f4 v[26:29], v[102:105], v[70:73], v[26:29] cbsz:4 blgp:4
	v_mfma_f32_16x16x128_f8f6f4 v[30:33], v[110:113], v[70:73], v[30:33] cbsz:4 blgp:4
	v_mfma_f32_16x16x128_f8f6f4 v[34:37], v[102:105], v[78:81], v[34:37] cbsz:4 blgp:4
	v_mfma_f32_16x16x128_f8f6f4 v[38:41], v[110:113], v[78:81], v[38:41] cbsz:4 blgp:4
	v_mfma_f32_16x16x128_f8f6f4 v[42:45], v[102:105], v[90:93], v[42:45] cbsz:4 blgp:4
	v_mfma_f32_16x16x128_f8f6f4 v[46:49], v[110:113], v[90:93], v[46:49] cbsz:4 blgp:4
	s_setprio 0
	s_barrier
	ds_read_b128 v[142:145], v161 offset:16384
	ds_read_b128 v[166:169], v161 offset:18432
	ds_read_b128 v[170:173], v162 offset:16384
	ds_read_b128 v[174:177], v162 offset:18432
	s_mov_b32 m0, s55
	s_nop 0
	global_load_lds_dwordx4 v148, s[48:49]
	s_mov_b32 m0, s56
	s_nop 0
	global_load_lds_dwordx4 v152, s[48:49]
	s_barrier
	s_waitcnt lgkmcnt(0)
	s_setprio 1
	v_mfma_f32_16x16x128_f8f6f4 v[50:53], v[142:145], v[58:61], v[6:9] cbsz:4 blgp:4
	v_mfma_f32_16x16x128_f8f6f4 v[54:57], v[166:169], v[58:61], v[2:5] cbsz:4 blgp:4
	v_mfma_f32_16x16x128_f8f6f4 v[50:53], v[170:173], v[62:65], v[50:53] cbsz:4 blgp:4
	v_mfma_f32_16x16x128_f8f6f4 v[54:57], v[174:177], v[62:65], v[54:57] cbsz:4 blgp:4
	v_mfma_f32_16x16x128_f8f6f4 v[58:61], v[142:145], v[66:69], v[6:9] cbsz:4 blgp:4
	v_mfma_f32_16x16x128_f8f6f4 v[62:65], v[166:169], v[66:69], v[2:5] cbsz:4 blgp:4
	v_mfma_f32_16x16x128_f8f6f4 v[58:61], v[170:173], v[70:73], v[58:61] cbsz:4 blgp:4
	v_mfma_f32_16x16x128_f8f6f4 v[62:65], v[174:177], v[70:73], v[62:65] cbsz:4 blgp:4
	v_mfma_f32_16x16x128_f8f6f4 v[66:69], v[142:145], v[74:77], v[6:9] cbsz:4 blgp:4
	v_mfma_f32_16x16x128_f8f6f4 v[70:73], v[166:169], v[74:77], v[2:5] cbsz:4 blgp:4
	v_mfma_f32_16x16x128_f8f6f4 v[66:69], v[170:173], v[78:81], v[66:69] cbsz:4 blgp:4
	v_mfma_f32_16x16x128_f8f6f4 v[70:73], v[174:177], v[78:81], v[70:73] cbsz:4 blgp:4
	v_mfma_f32_16x16x128_f8f6f4 v[74:77], v[142:145], v[86:89], v[6:9] cbsz:4 blgp:4
	v_mfma_f32_16x16x128_f8f6f4 v[78:81], v[166:169], v[86:89], v[2:5] cbsz:4 blgp:4
	v_mfma_f32_16x16x128_f8f6f4 v[74:77], v[170:173], v[90:93], v[74:77] cbsz:4 blgp:4
	v_mfma_f32_16x16x128_f8f6f4 v[78:81], v[174:177], v[90:93], v[78:81] cbsz:4 blgp:4
	s_setprio 0
	s_barrier
	ds_read_b128 v[114:117], v163 offset:16384
	ds_read_b128 v[122:125], v163 offset:18432
	ds_read_b128 v[130:133], v164 offset:16384
	ds_read_b128 v[134:137], v164 offset:18432
	ds_read_b128 v[178:181], v163 offset:20480
	ds_read_b128 v[182:185], v163 offset:22528
	ds_read_b128 v[186:189], v164 offset:20480
	ds_read_b128 v[190:193], v164 offset:22528
	s_mov_b32 m0, s54
	s_nop 0
	global_load_lds_dwordx4 v146, s[46:47]
	s_mov_b32 m0, s57
	s_nop 0
	global_load_lds_dwordx4 v150, s[46:47]
	s_barrier
	s_waitcnt lgkmcnt(0)
	s_setprio 1
	v_mfma_f32_16x16x128_f8f6f4 v[86:89], v[82:85], v[114:117], v[14:17] cbsz:4 blgp:4
	v_mfma_f32_16x16x128_f8f6f4 v[90:93], v[94:97], v[114:117], v[10:13] cbsz:4 blgp:4
	v_mfma_f32_16x16x128_f8f6f4 v[98:101], v[82:85], v[122:125], v[14:17] cbsz:4 blgp:4
	v_mfma_f32_16x16x128_f8f6f4 v[106:109], v[94:97], v[122:125], v[10:13] cbsz:4 blgp:4
	v_mfma_f32_16x16x128_f8f6f4 v[118:121], v[82:85], v[178:181], v[14:17] cbsz:4 blgp:4
	v_mfma_f32_16x16x128_f8f6f4 v[126:129], v[94:97], v[178:181], v[10:13] cbsz:4 blgp:4
	v_mfma_f32_16x16x128_f8f6f4 v[138:141], v[82:85], v[182:185], v[14:17] cbsz:4 blgp:4
	v_mfma_f32_16x16x128_f8f6f4 v[82:85], v[94:97], v[182:185], v[10:13] cbsz:4 blgp:4
	v_mfma_f32_16x16x128_f8f6f4 v[86:89], v[102:105], v[130:133], v[86:89] cbsz:4 blgp:4
	v_mfma_f32_16x16x128_f8f6f4 v[90:93], v[110:113], v[130:133], v[90:93] cbsz:4 blgp:4
	v_mfma_f32_16x16x128_f8f6f4 v[98:101], v[102:105], v[134:137], v[98:101] cbsz:4 blgp:4
	v_mfma_f32_16x16x128_f8f6f4 v[106:109], v[110:113], v[134:137], v[106:109] cbsz:4 blgp:4
	v_mfma_f32_16x16x128_f8f6f4 v[118:121], v[102:105], v[186:189], v[118:121] cbsz:4 blgp:4
	v_mfma_f32_16x16x128_f8f6f4 v[126:129], v[110:113], v[186:189], v[126:129] cbsz:4 blgp:4
	v_mfma_f32_16x16x128_f8f6f4 v[138:141], v[102:105], v[190:193], v[138:141] cbsz:4 blgp:4
	v_mfma_f32_16x16x128_f8f6f4 v[82:85], v[110:113], v[190:193], v[82:85] cbsz:4 blgp:4
	s_setprio 0
	s_barrier
	s_add_u32 s48, s48, s24
	s_addc_u32 s49, s49, s25
	s_mov_b32 m0, s58
	s_nop 0
	global_load_lds_dwordx4 v148, s[48:49]
	s_mov_b32 m0, s59
	s_nop 0
	global_load_lds_dwordx4 v152, s[48:49]
	s_waitcnt vmcnt(6)
	s_barrier
	s_setprio 1
	v_mfma_f32_16x16x128_f8f6f4 v[94:97], v[142:145], v[114:117], v[6:9] cbsz:4 blgp:4
	v_mfma_f32_16x16x128_f8f6f4 v[102:105], v[166:169], v[114:117], v[2:5] cbsz:4 blgp:4
	v_mfma_f32_16x16x128_f8f6f4 v[110:113], v[142:145], v[122:125], v[6:9] cbsz:4 blgp:4
	v_mfma_f32_16x16x128_f8f6f4 v[114:117], v[166:169], v[122:125], v[2:5] cbsz:4 blgp:4
	v_mfma_f32_16x16x128_f8f6f4 v[94:97], v[170:173], v[130:133], v[94:97] cbsz:4 blgp:4
	v_mfma_f32_16x16x128_f8f6f4 v[102:105], v[174:177], v[130:133], v[102:105] cbsz:4 blgp:4
	v_mfma_f32_16x16x128_f8f6f4 v[110:113], v[170:173], v[134:137], v[110:113] cbsz:4 blgp:4
	v_mfma_f32_16x16x128_f8f6f4 v[114:117], v[174:177], v[134:137], v[114:117] cbsz:4 blgp:4
	v_mfma_f32_16x16x128_f8f6f4 v[122:125], v[142:145], v[178:181], v[6:9] cbsz:4 blgp:4
	v_mfma_f32_16x16x128_f8f6f4 v[130:133], v[166:169], v[178:181], v[2:5] cbsz:4 blgp:4
	v_mfma_f32_16x16x128_f8f6f4 v[134:137], v[142:145], v[182:185], v[6:9] cbsz:4 blgp:4
	v_mfma_f32_16x16x128_f8f6f4 v[142:145], v[166:169], v[182:185], v[2:5] cbsz:4 blgp:4
	v_mfma_f32_16x16x128_f8f6f4 v[122:125], v[170:173], v[186:189], v[122:125] cbsz:4 blgp:4
	v_mfma_f32_16x16x128_f8f6f4 v[130:133], v[174:177], v[186:189], v[130:133] cbsz:4 blgp:4
	v_mfma_f32_16x16x128_f8f6f4 v[134:137], v[170:173], v[190:193], v[134:137] cbsz:4 blgp:4
	v_mfma_f32_16x16x128_f8f6f4 v[142:145], v[174:177], v[190:193], v[142:145] cbsz:4 blgp:4
	s_setprio 0
	s_barrier
	ds_read_b128 v[166:169], v161 offset:32768
	ds_read_b128 v[170:173], v161 offset:34816
	ds_read_b128 v[174:177], v162 offset:32768
	ds_read_b128 v[178:181], v162 offset:34816
	ds_read_b128 v[182:185], v163 offset:32768
	ds_read_b128 v[186:189], v163 offset:34816
	ds_read_b128 v[190:193], v164 offset:32768
	ds_read_b128 v[194:197], v164 offset:34816
	ds_read_b128 v[198:201], v163 offset:36864
	ds_read_b128 v[202:205], v163 offset:38912
	ds_read_b128 v[206:209], v164 offset:36864
	ds_read_b128 v[210:213], v164 offset:38912
	s_add_u32 s46, s46, s22
	s_addc_u32 s47, s47, s23
	s_mov_b32 m0, s60
	s_nop 0
	global_load_lds_dwordx4 v146, s[46:47]
	s_mov_b32 m0, s61
	s_nop 0
	global_load_lds_dwordx4 v150, s[46:47]
	s_waitcnt lgkmcnt(8)
	s_barrier
	s_waitcnt lgkmcnt(0)
	s_setprio 1
	v_mfma_f32_16x16x128_f8f6f4 v[18:21], v[166:169], v[182:185], v[18:21] cbsz:4 blgp:4
	v_mfma_f32_16x16x128_f8f6f4 v[22:25], v[170:173], v[182:185], v[22:25] cbsz:4 blgp:4
	v_mfma_f32_16x16x128_f8f6f4 v[26:29], v[166:169], v[186:189], v[26:29] cbsz:4 blgp:4
	v_mfma_f32_16x16x128_f8f6f4 v[30:33], v[170:173], v[186:189], v[30:33] cbsz:4 blgp:4
	v_mfma_f32_16x16x128_f8f6f4 v[34:37], v[166:169], v[198:201], v[34:37] cbsz:4 blgp:4
	v_mfma_f32_16x16x128_f8f6f4 v[38:41], v[170:173], v[198:201], v[38:41] cbsz:4 blgp:4
	v_mfma_f32_16x16x128_f8f6f4 v[42:45], v[166:169], v[202:205], v[42:45] cbsz:4 blgp:4
	v_mfma_f32_16x16x128_f8f6f4 v[46:49], v[170:173], v[202:205], v[46:49] cbsz:4 blgp:4
	v_mfma_f32_16x16x128_f8f6f4 v[18:21], v[174:177], v[190:193], v[18:21] cbsz:4 blgp:4
	v_mfma_f32_16x16x128_f8f6f4 v[22:25], v[178:181], v[190:193], v[22:25] cbsz:4 blgp:4
	v_mfma_f32_16x16x128_f8f6f4 v[26:29], v[174:177], v[194:197], v[26:29] cbsz:4 blgp:4
	v_mfma_f32_16x16x128_f8f6f4 v[30:33], v[178:181], v[194:197], v[30:33] cbsz:4 blgp:4
	v_mfma_f32_16x16x128_f8f6f4 v[34:37], v[174:177], v[206:209], v[34:37] cbsz:4 blgp:4
	v_mfma_f32_16x16x128_f8f6f4 v[38:41], v[178:181], v[206:209], v[38:41] cbsz:4 blgp:4
	v_mfma_f32_16x16x128_f8f6f4 v[42:45], v[174:177], v[210:213], v[42:45] cbsz:4 blgp:4
	v_mfma_f32_16x16x128_f8f6f4 v[46:49], v[178:181], v[210:213], v[46:49] cbsz:4 blgp:4
	s_setprio 0
	s_barrier
	ds_read_b128 v[214:217], v161 offset:49152
	ds_read_b128 v[218:221], v161 offset:51200
	ds_read_b128 v[222:225], v162 offset:49152
	ds_read_b128 v[226:229], v162 offset:51200
	s_mov_b32 m0, s64
	s_nop 0
	global_load_lds_dwordx4 v148, s[42:43]
	s_mov_b32 m0, s65
	s_nop 0
	global_load_lds_dwordx4 v152, s[42:43]
	s_barrier
	s_waitcnt lgkmcnt(0)
	s_setprio 1
	v_mfma_f32_16x16x128_f8f6f4 v[50:53], v[214:217], v[182:185], v[50:53] cbsz:4 blgp:4
	v_mfma_f32_16x16x128_f8f6f4 v[54:57], v[218:221], v[182:185], v[54:57] cbsz:4 blgp:4
	v_mfma_f32_16x16x128_f8f6f4 v[58:61], v[214:217], v[186:189], v[58:61] cbsz:4 blgp:4
	v_mfma_f32_16x16x128_f8f6f4 v[62:65], v[218:221], v[186:189], v[62:65] cbsz:4 blgp:4
	v_mfma_f32_16x16x128_f8f6f4 v[66:69], v[214:217], v[198:201], v[66:69] cbsz:4 blgp:4
	v_mfma_f32_16x16x128_f8f6f4 v[70:73], v[218:221], v[198:201], v[70:73] cbsz:4 blgp:4
	v_mfma_f32_16x16x128_f8f6f4 v[74:77], v[214:217], v[202:205], v[74:77] cbsz:4 blgp:4
	v_mfma_f32_16x16x128_f8f6f4 v[78:81], v[218:221], v[202:205], v[78:81] cbsz:4 blgp:4
	v_mfma_f32_16x16x128_f8f6f4 v[50:53], v[222:225], v[190:193], v[50:53] cbsz:4 blgp:4
	v_mfma_f32_16x16x128_f8f6f4 v[54:57], v[226:229], v[190:193], v[54:57] cbsz:4 blgp:4
	v_mfma_f32_16x16x128_f8f6f4 v[58:61], v[222:225], v[194:197], v[58:61] cbsz:4 blgp:4
	v_mfma_f32_16x16x128_f8f6f4 v[62:65], v[226:229], v[194:197], v[62:65] cbsz:4 blgp:4
	v_mfma_f32_16x16x128_f8f6f4 v[66:69], v[222:225], v[206:209], v[66:69] cbsz:4 blgp:4
	v_mfma_f32_16x16x128_f8f6f4 v[70:73], v[226:229], v[206:209], v[70:73] cbsz:4 blgp:4
	v_mfma_f32_16x16x128_f8f6f4 v[74:77], v[222:225], v[210:213], v[74:77] cbsz:4 blgp:4
	v_mfma_f32_16x16x128_f8f6f4 v[78:81], v[226:229], v[210:213], v[78:81] cbsz:4 blgp:4
	s_setprio 0
	s_barrier
	ds_read_b128 v[182:185], v163 offset:49152
	ds_read_b128 v[186:189], v163 offset:51200
	ds_read_b128 v[190:193], v164 offset:49152
	ds_read_b128 v[194:197], v164 offset:51200
	ds_read_b128 v[198:201], v163 offset:53248
	ds_read_b128 v[202:205], v163 offset:55296
	ds_read_b128 v[206:209], v164 offset:53248
	ds_read_b128 v[210:213], v164 offset:55296
	s_mov_b32 m0, s66
	s_nop 0
	global_load_lds_dwordx4 v146, s[44:45]
	s_mov_b32 m0, s67
	s_nop 0
	global_load_lds_dwordx4 v150, s[44:45]
	s_barrier
	s_waitcnt lgkmcnt(0)
	s_setprio 1
	v_mfma_f32_16x16x128_f8f6f4 v[86:89], v[166:169], v[182:185], v[86:89] cbsz:4 blgp:4
	v_mfma_f32_16x16x128_f8f6f4 v[90:93], v[170:173], v[182:185], v[90:93] cbsz:4 blgp:4
	v_mfma_f32_16x16x128_f8f6f4 v[98:101], v[166:169], v[186:189], v[98:101] cbsz:4 blgp:4
	v_mfma_f32_16x16x128_f8f6f4 v[106:109], v[170:173], v[186:189], v[106:109] cbsz:4 blgp:4
	v_mfma_f32_16x16x128_f8f6f4 v[118:121], v[166:169], v[198:201], v[118:121] cbsz:4 blgp:4
	v_mfma_f32_16x16x128_f8f6f4 v[126:129], v[170:173], v[198:201], v[126:129] cbsz:4 blgp:4
	v_mfma_f32_16x16x128_f8f6f4 v[138:141], v[166:169], v[202:205], v[138:141] cbsz:4 blgp:4
	v_mfma_f32_16x16x128_f8f6f4 v[82:85], v[170:173], v[202:205], v[82:85] cbsz:4 blgp:4
	v_mfma_f32_16x16x128_f8f6f4 v[86:89], v[174:177], v[190:193], v[86:89] cbsz:4 blgp:4
	v_mfma_f32_16x16x128_f8f6f4 v[90:93], v[178:181], v[190:193], v[90:93] cbsz:4 blgp:4
	v_mfma_f32_16x16x128_f8f6f4 v[98:101], v[174:177], v[194:197], v[98:101] cbsz:4 blgp:4
	v_mfma_f32_16x16x128_f8f6f4 v[106:109], v[178:181], v[194:197], v[106:109] cbsz:4 blgp:4
	v_mfma_f32_16x16x128_f8f6f4 v[118:121], v[174:177], v[206:209], v[118:121] cbsz:4 blgp:4
	v_mfma_f32_16x16x128_f8f6f4 v[126:129], v[178:181], v[206:209], v[126:129] cbsz:4 blgp:4
	v_mfma_f32_16x16x128_f8f6f4 v[138:141], v[174:177], v[210:213], v[138:141] cbsz:4 blgp:4
	v_mfma_f32_16x16x128_f8f6f4 v[82:85], v[178:181], v[210:213], v[82:85] cbsz:4 blgp:4
	s_setprio 0
	s_barrier
	s_add_u32 s42, s42, s24
	s_addc_u32 s43, s43, s25
	s_mov_b32 m0, s68
	s_nop 0
	global_load_lds_dwordx4 v148, s[42:43]
	s_mov_b32 m0, s69
	s_nop 0
	global_load_lds_dwordx4 v152, s[42:43]
	s_waitcnt vmcnt(6)
	s_barrier
	s_setprio 1
	v_mfma_f32_16x16x128_f8f6f4 v[94:97], v[214:217], v[182:185], v[94:97] cbsz:4 blgp:4
	v_mfma_f32_16x16x128_f8f6f4 v[102:105], v[218:221], v[182:185], v[102:105] cbsz:4 blgp:4
	v_mfma_f32_16x16x128_f8f6f4 v[110:113], v[214:217], v[186:189], v[110:113] cbsz:4 blgp:4
	v_mfma_f32_16x16x128_f8f6f4 v[114:117], v[218:221], v[186:189], v[114:117] cbsz:4 blgp:4
	v_mfma_f32_16x16x128_f8f6f4 v[122:125], v[214:217], v[198:201], v[122:125] cbsz:4 blgp:4
	v_mfma_f32_16x16x128_f8f6f4 v[130:133], v[218:221], v[198:201], v[130:133] cbsz:4 blgp:4
	v_mfma_f32_16x16x128_f8f6f4 v[134:137], v[214:217], v[202:205], v[134:137] cbsz:4 blgp:4
	v_mfma_f32_16x16x128_f8f6f4 v[142:145], v[218:221], v[202:205], v[142:145] cbsz:4 blgp:4
	v_mfma_f32_16x16x128_f8f6f4 v[94:97], v[222:225], v[190:193], v[94:97] cbsz:4 blgp:4
	v_mfma_f32_16x16x128_f8f6f4 v[102:105], v[226:229], v[190:193], v[102:105] cbsz:4 blgp:4
	v_mfma_f32_16x16x128_f8f6f4 v[110:113], v[222:225], v[194:197], v[110:113] cbsz:4 blgp:4
	v_mfma_f32_16x16x128_f8f6f4 v[114:117], v[226:229], v[194:197], v[114:117] cbsz:4 blgp:4
	v_mfma_f32_16x16x128_f8f6f4 v[122:125], v[222:225], v[206:209], v[122:125] cbsz:4 blgp:4
	v_mfma_f32_16x16x128_f8f6f4 v[130:133], v[226:229], v[206:209], v[130:133] cbsz:4 blgp:4
	v_mfma_f32_16x16x128_f8f6f4 v[134:137], v[222:225], v[210:213], v[134:137] cbsz:4 blgp:4
	v_mfma_f32_16x16x128_f8f6f4 v[142:145], v[226:229], v[210:213], v[142:145] cbsz:4 blgp:4
	s_setprio 0
	s_andn2_b64 vcc, exec, s[34:35]
	s_barrier
	s_cbranch_vccnz .LBB4_4
	s_ashr_i32 s29, s28, 31
	s_lshl_b64 s[42:43], s[28:29], 10
	s_add_u32 s42, s10, s42
	s_addc_u32 s43, s11, s43
	s_add_u32 s29, s40, 0x200
	s_addc_u32 s78, s41, 0
	s_add_u32 s79, s38, 0x200
	s_addc_u32 s80, s39, 0
	s_add_u32 s38, s81, 0x180
	s_addc_u32 s39, s82, 0
	s_mov_b32 s81, 4
	s_cmp_eq_u32 s63, s81
	s_cselect_b64 s[40:41], -1, 0
	s_cmp_lg_u32 s63, s81
	s_cbranch_scc1 .LBB4_15

.LBB4_15:
	ds_read_b128 v[166:169], v161
	ds_read_b128 v[170:173], v161 offset:2048
	ds_read_b128 v[174:177], v162
	ds_read_b128 v[178:181], v162 offset:2048
	s_and_b64 s[40:41], s[40:41], exec
	s_cselect_b32 s46, s36, s29
	s_cselect_b32 s47, s37, s78
	s_cselect_b32 s49, s5, s80
	s_cselect_b32 s48, s4, s79
	s_add_u32 s44, s46, 0x80
	s_addc_u32 s45, s47, 0
	s_add_u32 s40, s48, 0x80
	s_addc_u32 s41, s49, 0
	ds_read_b128 v[182:185], v163
	ds_read_b128 v[186:189], v163 offset:2048
	ds_read_b128 v[190:193], v164
	ds_read_b128 v[194:197], v164 offset:2048
	ds_read_b128 v[198:201], v163 offset:4096
	ds_read_b128 v[202:205], v163 offset:6144
	ds_read_b128 v[206:209], v164 offset:4096
	ds_read_b128 v[210:213], v164 offset:6144
	s_mov_b32 m0, s70
	s_nop 0
	global_load_lds_dwordx4 v146, s[38:39]
	s_mov_b32 m0, s71
	s_nop 0
	global_load_lds_dwordx4 v150, s[38:39]
	s_waitcnt lgkmcnt(8)
	s_barrier
	s_waitcnt lgkmcnt(0)
	s_setprio 1
	v_mfma_f32_16x16x128_f8f6f4 v[18:21], v[166:169], v[182:185], v[18:21] cbsz:4 blgp:4
	v_mfma_f32_16x16x128_f8f6f4 v[22:25], v[170:173], v[182:185], v[22:25] cbsz:4 blgp:4
	v_mfma_f32_16x16x128_f8f6f4 v[26:29], v[166:169], v[186:189], v[26:29] cbsz:4 blgp:4
	v_mfma_f32_16x16x128_f8f6f4 v[30:33], v[170:173], v[186:189], v[30:33] cbsz:4 blgp:4
	v_mfma_f32_16x16x128_f8f6f4 v[34:37], v[166:169], v[198:201], v[34:37] cbsz:4 blgp:4
	v_mfma_f32_16x16x128_f8f6f4 v[38:41], v[170:173], v[198:201], v[38:41] cbsz:4 blgp:4
	v_mfma_f32_16x16x128_f8f6f4 v[42:45], v[166:169], v[202:205], v[42:45] cbsz:4 blgp:4
	v_mfma_f32_16x16x128_f8f6f4 v[46:49], v[170:173], v[202:205], v[46:49] cbsz:4 blgp:4
	v_mfma_f32_16x16x128_f8f6f4 v[18:21], v[174:177], v[190:193], v[18:21] cbsz:4 blgp:4
	v_mfma_f32_16x16x128_f8f6f4 v[22:25], v[178:181], v[190:193], v[22:25] cbsz:4 blgp:4
	v_mfma_f32_16x16x128_f8f6f4 v[26:29], v[174:177], v[194:197], v[26:29] cbsz:4 blgp:4
	v_mfma_f32_16x16x128_f8f6f4 v[30:33], v[178:181], v[194:197], v[30:33] cbsz:4 blgp:4
	v_mfma_f32_16x16x128_f8f6f4 v[34:37], v[174:177], v[206:209], v[34:37] cbsz:4 blgp:4
	v_mfma_f32_16x16x128_f8f6f4 v[38:41], v[178:181], v[206:209], v[38:41] cbsz:4 blgp:4
	v_mfma_f32_16x16x128_f8f6f4 v[42:45], v[174:177], v[210:213], v[42:45] cbsz:4 blgp:4
	v_mfma_f32_16x16x128_f8f6f4 v[46:49], v[178:181], v[210:213], v[46:49] cbsz:4 blgp:4
	s_setprio 0
	s_barrier
	ds_read_b128 v[214:217], v161 offset:16384
	ds_read_b128 v[218:221], v161 offset:18432
	ds_read_b128 v[222:225], v162 offset:16384
	ds_read_b128 v[226:229], v162 offset:18432
	s_mov_b32 m0, s55
	s_nop 0
	global_load_lds_dwordx4 v148, s[48:49]
	s_mov_b32 m0, s56
	s_nop 0
	global_load_lds_dwordx4 v152, s[48:49]
	s_barrier
	s_waitcnt lgkmcnt(0)
	s_setprio 1
	v_mfma_f32_16x16x128_f8f6f4 v[50:53], v[214:217], v[182:185], v[50:53] cbsz:4 blgp:4
	v_mfma_f32_16x16x128_f8f6f4 v[54:57], v[218:221], v[182:185], v[54:57] cbsz:4 blgp:4
	v_mfma_f32_16x16x128_f8f6f4 v[58:61], v[214:217], v[186:189], v[58:61] cbsz:4 blgp:4
	v_mfma_f32_16x16x128_f8f6f4 v[62:65], v[218:221], v[186:189], v[62:65] cbsz:4 blgp:4
	v_mfma_f32_16x16x128_f8f6f4 v[66:69], v[214:217], v[198:201], v[66:69] cbsz:4 blgp:4
	v_mfma_f32_16x16x128_f8f6f4 v[70:73], v[218:221], v[198:201], v[70:73] cbsz:4 blgp:4
	v_mfma_f32_16x16x128_f8f6f4 v[74:77], v[214:217], v[202:205], v[74:77] cbsz:4 blgp:4
	v_mfma_f32_16x16x128_f8f6f4 v[78:81], v[218:221], v[202:205], v[78:81] cbsz:4 blgp:4
	v_mfma_f32_16x16x128_f8f6f4 v[50:53], v[222:225], v[190:193], v[50:53] cbsz:4 blgp:4
	v_mfma_f32_16x16x128_f8f6f4 v[54:57], v[226:229], v[190:193], v[54:57] cbsz:4 blgp:4
	v_mfma_f32_16x16x128_f8f6f4 v[58:61], v[222:225], v[194:197], v[58:61] cbsz:4 blgp:4
	v_mfma_f32_16x16x128_f8f6f4 v[62:65], v[226:229], v[194:197], v[62:65] cbsz:4 blgp:4
	v_mfma_f32_16x16x128_f8f6f4 v[66:69], v[222:225], v[206:209], v[66:69] cbsz:4 blgp:4
	v_mfma_f32_16x16x128_f8f6f4 v[70:73], v[226:229], v[206:209], v[70:73] cbsz:4 blgp:4
	v_mfma_f32_16x16x128_f8f6f4 v[74:77], v[222:225], v[210:213], v[74:77] cbsz:4 blgp:4
	v_mfma_f32_16x16x128_f8f6f4 v[78:81], v[226:229], v[210:213], v[78:81] cbsz:4 blgp:4
	s_setprio 0
	s_barrier
	ds_read_b128 v[182:185], v163 offset:16384
	ds_read_b128 v[186:189], v163 offset:18432
	ds_read_b128 v[190:193], v164 offset:16384
	ds_read_b128 v[194:197], v164 offset:18432
	ds_read_b128 v[198:201], v163 offset:20480
	ds_read_b128 v[202:205], v163 offset:22528
	ds_read_b128 v[206:209], v164 offset:20480
	ds_read_b128 v[210:213], v164 offset:22528
	s_mov_b32 m0, s54
	s_nop 0
	global_load_lds_dwordx4 v146, s[46:47]
	s_mov_b32 m0, s57
	s_nop 0
	global_load_lds_dwordx4 v150, s[46:47]
	s_barrier
	s_waitcnt lgkmcnt(0)
	s_setprio 1
	v_mfma_f32_16x16x128_f8f6f4 v[86:89], v[166:169], v[182:185], v[86:89] cbsz:4 blgp:4
	v_mfma_f32_16x16x128_f8f6f4 v[90:93], v[170:173], v[182:185], v[90:93] cbsz:4 blgp:4
	v_mfma_f32_16x16x128_f8f6f4 v[98:101], v[166:169], v[186:189], v[98:101] cbsz:4 blgp:4
	v_mfma_f32_16x16x128_f8f6f4 v[106:109], v[170:173], v[186:189], v[106:109] cbsz:4 blgp:4
	v_mfma_f32_16x16x128_f8f6f4 v[118:121], v[166:169], v[198:201], v[118:121] cbsz:4 blgp:4
	v_mfma_f32_16x16x128_f8f6f4 v[126:129], v[170:173], v[198:201], v[126:129] cbsz:4 blgp:4
	v_mfma_f32_16x16x128_f8f6f4 v[138:141], v[166:169], v[202:205], v[138:141] cbsz:4 blgp:4
	v_mfma_f32_16x16x128_f8f6f4 v[82:85], v[170:173], v[202:205], v[82:85] cbsz:4 blgp:4
	v_mfma_f32_16x16x128_f8f6f4 v[86:89], v[174:177], v[190:193], v[86:89] cbsz:4 blgp:4
	v_mfma_f32_16x16x128_f8f6f4 v[90:93], v[178:181], v[190:193], v[90:93] cbsz:4 blgp:4
	v_mfma_f32_16x16x128_f8f6f4 v[98:101], v[174:177], v[194:197], v[98:101] cbsz:4 blgp:4
	v_mfma_f32_16x16x128_f8f6f4 v[106:109], v[178:181], v[194:197], v[106:109] cbsz:4 blgp:4
	v_mfma_f32_16x16x128_f8f6f4 v[118:121], v[174:177], v[206:209], v[118:121] cbsz:4 blgp:4
	v_mfma_f32_16x16x128_f8f6f4 v[126:129], v[178:181], v[206:209], v[126:129] cbsz:4 blgp:4
	v_mfma_f32_16x16x128_f8f6f4 v[138:141], v[174:177], v[210:213], v[138:141] cbsz:4 blgp:4
	v_mfma_f32_16x16x128_f8f6f4 v[82:85], v[178:181], v[210:213], v[82:85] cbsz:4 blgp:4
	s_setprio 0
	s_barrier
	s_add_u32 s48, s48, s24
	s_addc_u32 s49, s49, s25
	s_mov_b32 m0, s58
	s_nop 0
	global_load_lds_dwordx4 v148, s[48:49]
	s_mov_b32 m0, s59
	s_nop 0
	global_load_lds_dwordx4 v152, s[48:49]
	s_waitcnt vmcnt(6)
	s_barrier
	s_setprio 1
	v_mfma_f32_16x16x128_f8f6f4 v[94:97], v[214:217], v[182:185], v[94:97] cbsz:4 blgp:4
	v_mfma_f32_16x16x128_f8f6f4 v[102:105], v[218:221], v[182:185], v[102:105] cbsz:4 blgp:4
	v_mfma_f32_16x16x128_f8f6f4 v[110:113], v[214:217], v[186:189], v[110:113] cbsz:4 blgp:4
	v_mfma_f32_16x16x128_f8f6f4 v[114:117], v[218:221], v[186:189], v[114:117] cbsz:4 blgp:4
	v_mfma_f32_16x16x128_f8f6f4 v[122:125], v[214:217], v[198:201], v[122:125] cbsz:4 blgp:4
	v_mfma_f32_16x16x128_f8f6f4 v[130:133], v[218:221], v[198:201], v[130:133] cbsz:4 blgp:4
	v_mfma_f32_16x16x128_f8f6f4 v[134:137], v[214:217], v[202:205], v[134:137] cbsz:4 blgp:4
	v_mfma_f32_16x16x128_f8f6f4 v[142:145], v[218:221], v[202:205], v[142:145] cbsz:4 blgp:4
	v_mfma_f32_16x16x128_f8f6f4 v[94:97], v[222:225], v[190:193], v[94:97] cbsz:4 blgp:4
	v_mfma_f32_16x16x128_f8f6f4 v[102:105], v[226:229], v[190:193], v[102:105] cbsz:4 blgp:4
	v_mfma_f32_16x16x128_f8f6f4 v[110:113], v[222:225], v[194:197], v[110:113] cbsz:4 blgp:4
	v_mfma_f32_16x16x128_f8f6f4 v[114:117], v[226:229], v[194:197], v[114:117] cbsz:4 blgp:4
	v_mfma_f32_16x16x128_f8f6f4 v[122:125], v[222:225], v[206:209], v[122:125] cbsz:4 blgp:4
	v_mfma_f32_16x16x128_f8f6f4 v[130:133], v[226:229], v[206:209], v[130:133] cbsz:4 blgp:4
	v_mfma_f32_16x16x128_f8f6f4 v[134:137], v[222:225], v[210:213], v[134:137] cbsz:4 blgp:4
	v_mfma_f32_16x16x128_f8f6f4 v[142:145], v[226:229], v[210:213], v[142:145] cbsz:4 blgp:4
	s_setprio 0
	s_barrier
	ds_read_b128 v[166:169], v161 offset:32768
	ds_read_b128 v[170:173], v161 offset:34816
	ds_read_b128 v[174:177], v162 offset:32768
	ds_read_b128 v[178:181], v162 offset:34816
	ds_read_b128 v[182:185], v163 offset:32768
	ds_read_b128 v[186:189], v163 offset:34816
	ds_read_b128 v[190:193], v164 offset:32768
	ds_read_b128 v[194:197], v164 offset:34816
	ds_read_b128 v[198:201], v163 offset:36864
	ds_read_b128 v[202:205], v163 offset:38912
	ds_read_b128 v[206:209], v164 offset:36864
	ds_read_b128 v[210:213], v164 offset:38912
	s_add_u32 s46, s46, s22
	s_addc_u32 s47, s47, s23
	s_mov_b32 m0, s60
	s_nop 0
	global_load_lds_dwordx4 v146, s[46:47]
	s_mov_b32 m0, s61
	s_nop 0
	global_load_lds_dwordx4 v150, s[46:47]
	s_waitcnt lgkmcnt(8)
	s_barrier
	s_waitcnt lgkmcnt(0)
	s_setprio 1
	v_mfma_f32_16x16x128_f8f6f4 v[18:21], v[166:169], v[182:185], v[18:21] cbsz:4 blgp:4
	v_mfma_f32_16x16x128_f8f6f4 v[22:25], v[170:173], v[182:185], v[22:25] cbsz:4 blgp:4
	v_mfma_f32_16x16x128_f8f6f4 v[26:29], v[166:169], v[186:189], v[26:29] cbsz:4 blgp:4
	v_mfma_f32_16x16x128_f8f6f4 v[30:33], v[170:173], v[186:189], v[30:33] cbsz:4 blgp:4
	v_mfma_f32_16x16x128_f8f6f4 v[34:37], v[166:169], v[198:201], v[34:37] cbsz:4 blgp:4
	v_mfma_f32_16x16x128_f8f6f4 v[38:41], v[170:173], v[198:201], v[38:41] cbsz:4 blgp:4
	v_mfma_f32_16x16x128_f8f6f4 v[42:45], v[166:169], v[202:205], v[42:45] cbsz:4 blgp:4
	v_mfma_f32_16x16x128_f8f6f4 v[46:49], v[170:173], v[202:205], v[46:49] cbsz:4 blgp:4
	v_mfma_f32_16x16x128_f8f6f4 v[18:21], v[174:177], v[190:193], v[18:21] cbsz:4 blgp:4
	v_mfma_f32_16x16x128_f8f6f4 v[22:25], v[178:181], v[190:193], v[22:25] cbsz:4 blgp:4
	v_mfma_f32_16x16x128_f8f6f4 v[26:29], v[174:177], v[194:197], v[26:29] cbsz:4 blgp:4
	v_mfma_f32_16x16x128_f8f6f4 v[30:33], v[178:181], v[194:197], v[30:33] cbsz:4 blgp:4
	v_mfma_f32_16x16x128_f8f6f4 v[34:37], v[174:177], v[206:209], v[34:37] cbsz:4 blgp:4
	v_mfma_f32_16x16x128_f8f6f4 v[38:41], v[178:181], v[206:209], v[38:41] cbsz:4 blgp:4
	v_mfma_f32_16x16x128_f8f6f4 v[42:45], v[174:177], v[210:213], v[42:45] cbsz:4 blgp:4
	v_mfma_f32_16x16x128_f8f6f4 v[46:49], v[178:181], v[210:213], v[46:49] cbsz:4 blgp:4
	s_setprio 0
	s_barrier
	ds_read_b128 v[214:217], v161 offset:49152
	ds_read_b128 v[218:221], v161 offset:51200
	ds_read_b128 v[222:225], v162 offset:49152
	ds_read_b128 v[226:229], v162 offset:51200
	s_mov_b32 m0, s64
	s_nop 0
	global_load_lds_dwordx4 v148, s[40:41]
	s_mov_b32 m0, s65
	s_nop 0
	global_load_lds_dwordx4 v152, s[40:41]
	s_barrier
	s_waitcnt lgkmcnt(0)
	s_setprio 1
	v_mfma_f32_16x16x128_f8f6f4 v[50:53], v[214:217], v[182:185], v[50:53] cbsz:4 blgp:4
	v_mfma_f32_16x16x128_f8f6f4 v[54:57], v[218:221], v[182:185], v[54:57] cbsz:4 blgp:4
	v_mfma_f32_16x16x128_f8f6f4 v[58:61], v[214:217], v[186:189], v[58:61] cbsz:4 blgp:4
	v_mfma_f32_16x16x128_f8f6f4 v[62:65], v[218:221], v[186:189], v[62:65] cbsz:4 blgp:4
	v_mfma_f32_16x16x128_f8f6f4 v[66:69], v[214:217], v[198:201], v[66:69] cbsz:4 blgp:4
	v_mfma_f32_16x16x128_f8f6f4 v[70:73], v[218:221], v[198:201], v[70:73] cbsz:4 blgp:4
	v_mfma_f32_16x16x128_f8f6f4 v[74:77], v[214:217], v[202:205], v[74:77] cbsz:4 blgp:4
	v_mfma_f32_16x16x128_f8f6f4 v[78:81], v[218:221], v[202:205], v[78:81] cbsz:4 blgp:4
	v_mfma_f32_16x16x128_f8f6f4 v[50:53], v[222:225], v[190:193], v[50:53] cbsz:4 blgp:4
	v_mfma_f32_16x16x128_f8f6f4 v[54:57], v[226:229], v[190:193], v[54:57] cbsz:4 blgp:4
	v_mfma_f32_16x16x128_f8f6f4 v[58:61], v[222:225], v[194:197], v[58:61] cbsz:4 blgp:4
	v_mfma_f32_16x16x128_f8f6f4 v[62:65], v[226:229], v[194:197], v[62:65] cbsz:4 blgp:4
	v_mfma_f32_16x16x128_f8f6f4 v[66:69], v[222:225], v[206:209], v[66:69] cbsz:4 blgp:4
	v_mfma_f32_16x16x128_f8f6f4 v[70:73], v[226:229], v[206:209], v[70:73] cbsz:4 blgp:4
	v_mfma_f32_16x16x128_f8f6f4 v[74:77], v[222:225], v[210:213], v[74:77] cbsz:4 blgp:4
	v_mfma_f32_16x16x128_f8f6f4 v[78:81], v[226:229], v[210:213], v[78:81] cbsz:4 blgp:4
	s_setprio 0
	s_barrier
	ds_read_b128 v[182:185], v163 offset:49152
	ds_read_b128 v[186:189], v163 offset:51200
	ds_read_b128 v[190:193], v164 offset:49152
	ds_read_b128 v[194:197], v164 offset:51200
	ds_read_b128 v[198:201], v163 offset:53248
	ds_read_b128 v[202:205], v163 offset:55296
	ds_read_b128 v[206:209], v164 offset:53248
	ds_read_b128 v[210:213], v164 offset:55296
	s_mov_b32 m0, s66
	s_nop 0
	global_load_lds_dwordx4 v146, s[44:45]
	s_mov_b32 m0, s67
	s_nop 0
	global_load_lds_dwordx4 v150, s[44:45]
	s_barrier
	s_waitcnt lgkmcnt(0)
	s_setprio 1
	v_mfma_f32_16x16x128_f8f6f4 v[86:89], v[166:169], v[182:185], v[86:89] cbsz:4 blgp:4
	v_mfma_f32_16x16x128_f8f6f4 v[90:93], v[170:173], v[182:185], v[90:93] cbsz:4 blgp:4
	v_mfma_f32_16x16x128_f8f6f4 v[98:101], v[166:169], v[186:189], v[98:101] cbsz:4 blgp:4
	v_mfma_f32_16x16x128_f8f6f4 v[106:109], v[170:173], v[186:189], v[106:109] cbsz:4 blgp:4
	v_mfma_f32_16x16x128_f8f6f4 v[118:121], v[166:169], v[198:201], v[118:121] cbsz:4 blgp:4
	v_mfma_f32_16x16x128_f8f6f4 v[126:129], v[170:173], v[198:201], v[126:129] cbsz:4 blgp:4
	v_mfma_f32_16x16x128_f8f6f4 v[138:141], v[166:169], v[202:205], v[138:141] cbsz:4 blgp:4
	v_mfma_f32_16x16x128_f8f6f4 v[82:85], v[170:173], v[202:205], v[82:85] cbsz:4 blgp:4
	v_mfma_f32_16x16x128_f8f6f4 v[86:89], v[174:177], v[190:193], v[86:89] cbsz:4 blgp:4
	v_mfma_f32_16x16x128_f8f6f4 v[90:93], v[178:181], v[190:193], v[90:93] cbsz:4 blgp:4
	v_mfma_f32_16x16x128_f8f6f4 v[98:101], v[174:177], v[194:197], v[98:101] cbsz:4 blgp:4
	v_mfma_f32_16x16x128_f8f6f4 v[106:109], v[178:181], v[194:197], v[106:109] cbsz:4 blgp:4
	v_mfma_f32_16x16x128_f8f6f4 v[118:121], v[174:177], v[206:209], v[118:121] cbsz:4 blgp:4
	v_mfma_f32_16x16x128_f8f6f4 v[126:129], v[178:181], v[206:209], v[126:129] cbsz:4 blgp:4
	v_mfma_f32_16x16x128_f8f6f4 v[138:141], v[174:177], v[210:213], v[138:141] cbsz:4 blgp:4
	v_mfma_f32_16x16x128_f8f6f4 v[82:85], v[178:181], v[210:213], v[82:85] cbsz:4 blgp:4
	s_setprio 0
	s_barrier
	s_add_u32 s40, s40, s24
	s_addc_u32 s41, s41, s25
	s_mov_b32 m0, s68
	s_nop 0
	global_load_lds_dwordx4 v148, s[40:41]
	s_mov_b32 m0, s69
	s_nop 0
	global_load_lds_dwordx4 v152, s[40:41]
	s_waitcnt vmcnt(6)
	s_barrier
	s_setprio 1
	v_mfma_f32_16x16x128_f8f6f4 v[94:97], v[214:217], v[182:185], v[94:97] cbsz:4 blgp:4
	v_mfma_f32_16x16x128_f8f6f4 v[102:105], v[218:221], v[182:185], v[102:105] cbsz:4 blgp:4
	v_mfma_f32_16x16x128_f8f6f4 v[110:113], v[214:217], v[186:189], v[110:113] cbsz:4 blgp:4
	v_mfma_f32_16x16x128_f8f6f4 v[114:117], v[218:221], v[186:189], v[114:117] cbsz:4 blgp:4
	v_mfma_f32_16x16x128_f8f6f4 v[122:125], v[214:217], v[198:201], v[122:125] cbsz:4 blgp:4
	v_mfma_f32_16x16x128_f8f6f4 v[130:133], v[218:221], v[198:201], v[130:133] cbsz:4 blgp:4
	v_mfma_f32_16x16x128_f8f6f4 v[134:137], v[214:217], v[202:205], v[134:137] cbsz:4 blgp:4
	v_mfma_f32_16x16x128_f8f6f4 v[142:145], v[218:221], v[202:205], v[142:145] cbsz:4 blgp:4
	v_mfma_f32_16x16x128_f8f6f4 v[94:97], v[222:225], v[190:193], v[94:97] cbsz:4 blgp:4
	v_mfma_f32_16x16x128_f8f6f4 v[102:105], v[226:229], v[190:193], v[102:105] cbsz:4 blgp:4
	v_mfma_f32_16x16x128_f8f6f4 v[110:113], v[222:225], v[194:197], v[110:113] cbsz:4 blgp:4
	v_mfma_f32_16x16x128_f8f6f4 v[114:117], v[226:229], v[194:197], v[114:117] cbsz:4 blgp:4
	v_mfma_f32_16x16x128_f8f6f4 v[122:125], v[222:225], v[206:209], v[122:125] cbsz:4 blgp:4
	v_mfma_f32_16x16x128_f8f6f4 v[130:133], v[226:229], v[206:209], v[130:133] cbsz:4 blgp:4
	v_mfma_f32_16x16x128_f8f6f4 v[134:137], v[222:225], v[210:213], v[134:137] cbsz:4 blgp:4
	v_mfma_f32_16x16x128_f8f6f4 v[142:145], v[226:229], v[210:213], v[142:145] cbsz:4 blgp:4
	s_setprio 0
	s_add_i32 s40, s81, 2
	s_add_u32 s29, s29, 0x100
	s_addc_u32 s78, s78, 0
	s_add_u32 s79, s79, 0x100
	s_addc_u32 s80, s80, 0
	s_add_u32 s38, s38, 0x100
	s_addc_u32 s39, s39, 0
	s_cmp_ge_i32 s81, s63
	s_barrier
	s_cbranch_scc1 .LBB4_4
	s_mov_b32 s81, s40
	s_cmp_eq_u32 s63, s81
	s_cselect_b64 s[40:41], -1, 0
	s_cmp_lg_u32 s63, s81
	s_cbranch_scc0 .LBB4_14
	s_branch .LBB4_15

.LBB5_12:
	s_add_u32 s82, s42, s22
	s_addc_u32 s83, s43, s23
	s_add_u32 s29, s42, 0x100
	s_addc_u32 s46, s43, 0
	s_and_b64 s[44:45], s[14:15], exec
	ds_read_b128 v[82:85], v163
	ds_read_b128 v[94:97], v163 offset:2048
	ds_read_b128 v[102:105], v164
	ds_read_b128 v[110:113], v164 offset:2048
	s_cselect_b32 s49, s39, s46
	s_cselect_b32 s48, s38, s29
	s_add_u32 s29, s40, 0x100
	s_addc_u32 s46, s41, 0
	s_and_b64 s[44:45], s[14:15], exec
	s_cselect_b32 s51, s5, s46
	s_cselect_b32 s50, s4, s29
	s_add_u32 s46, s48, 0x80
	s_addc_u32 s47, s49, 0
	s_add_u32 s44, s50, 0x80
	s_addc_u32 s45, s51, 0
	ds_read_b128 v[58:61], v165
	ds_read_b128 v[66:69], v165 offset:2048
	ds_read_b128 v[62:65], v166
	ds_read_b128 v[70:73], v166 offset:2048
	ds_read_b128 v[74:77], v165 offset:4096
	ds_read_b128 v[86:89], v165 offset:6144
	ds_read_b128 v[78:81], v166 offset:4096
	ds_read_b128 v[90:93], v166 offset:6144
	s_add_u32 s80, s82, 0x80
	s_addc_u32 s81, s83, 0
	s_mov_b32 m0, s71
	s_nop 0
	global_load_lds_dwordx4 v146, s[80:81]
	s_mov_b32 m0, s72
	s_nop 0
	global_load_lds_dwordx4 v150, s[80:81]
	s_waitcnt lgkmcnt(8)
	s_barrier
	s_waitcnt lgkmcnt(0)
	s_waitcnt vmcnt(16)
	v_mov_b32_e32 v1, v0
	v_pk_mul_f32 v[16:17], v[0:1], v[16:17]
	v_pk_mul_f32 v[14:15], v[154:155], v[14:15]
	v_pk_mul_f32 v[12:13], v[0:1], v[12:13]
	v_pk_mul_f32 v[10:11], v[154:155], v[10:11]
	v_pk_mul_f32 v[8:9], v[0:1], v[8:9]
	v_pk_mul_f32 v[6:7], v[154:155], v[6:7]
	v_pk_mul_f32 v[4:5], v[0:1], v[4:5]
	v_pk_mul_f32 v[2:3], v[154:155], v[2:3]
	s_setprio 1
	v_mfma_f32_16x16x128_f8f6f4 v[18:21], v[82:85], v[58:61], v[14:17] cbsz:4 blgp:4
	v_mfma_f32_16x16x128_f8f6f4 v[22:25], v[94:97], v[58:61], v[10:13] cbsz:4 blgp:4
	v_mfma_f32_16x16x128_f8f6f4 v[26:29], v[82:85], v[66:69], v[14:17] cbsz:4 blgp:4
	v_mfma_f32_16x16x128_f8f6f4 v[30:33], v[94:97], v[66:69], v[10:13] cbsz:4 blgp:4
	v_mfma_f32_16x16x128_f8f6f4 v[34:37], v[82:85], v[74:77], v[14:17] cbsz:4 blgp:4
	v_mfma_f32_16x16x128_f8f6f4 v[38:41], v[94:97], v[74:77], v[10:13] cbsz:4 blgp:4
	v_mfma_f32_16x16x128_f8f6f4 v[42:45], v[82:85], v[86:89], v[14:17] cbsz:4 blgp:4
	v_mfma_f32_16x16x128_f8f6f4 v[46:49], v[94:97], v[86:89], v[10:13] cbsz:4 blgp:4
	v_mfma_f32_16x16x128_f8f6f4 v[18:21], v[102:105], v[62:65], v[18:21] cbsz:4 blgp:4
	v_mfma_f32_16x16x128_f8f6f4 v[22:25], v[110:113], v[62:65], v[22:25] cbsz:4 blgp:4
	v_mfma_f32_16x16x128_f8f6f4 v[26:29], v[102:105], v[70:73], v[26:29] cbsz:4 blgp:4
	v_mfma_f32_16x16x128_f8f6f4 v[30:33], v[110:113], v[70:73], v[30:33] cbsz:4 blgp:4
	v_mfma_f32_16x16x128_f8f6f4 v[34:37], v[102:105], v[78:81], v[34:37] cbsz:4 blgp:4
	v_mfma_f32_16x16x128_f8f6f4 v[38:41], v[110:113], v[78:81], v[38:41] cbsz:4 blgp:4
	v_mfma_f32_16x16x128_f8f6f4 v[42:45], v[102:105], v[90:93], v[42:45] cbsz:4 blgp:4
	v_mfma_f32_16x16x128_f8f6f4 v[46:49], v[110:113], v[90:93], v[46:49] cbsz:4 blgp:4
	s_setprio 0
	s_barrier
	ds_read_b128 v[142:145], v163 offset:16384
	ds_read_b128 v[156:159], v163 offset:18432
	ds_read_b128 v[168:171], v164 offset:16384
	ds_read_b128 v[172:175], v164 offset:18432
	s_mov_b32 m0, s56
	s_nop 0
	global_load_lds_dwordx4 v148, s[50:51]
	s_mov_b32 m0, s57
	s_nop 0
	global_load_lds_dwordx4 v152, s[50:51]
	s_barrier
	s_waitcnt lgkmcnt(0)
	s_setprio 1
	v_mfma_f32_16x16x128_f8f6f4 v[50:53], v[142:145], v[58:61], v[6:9] cbsz:4 blgp:4
	v_mfma_f32_16x16x128_f8f6f4 v[54:57], v[156:159], v[58:61], v[2:5] cbsz:4 blgp:4
	v_mfma_f32_16x16x128_f8f6f4 v[50:53], v[168:171], v[62:65], v[50:53] cbsz:4 blgp:4
	v_mfma_f32_16x16x128_f8f6f4 v[54:57], v[172:175], v[62:65], v[54:57] cbsz:4 blgp:4
	v_mfma_f32_16x16x128_f8f6f4 v[58:61], v[142:145], v[66:69], v[6:9] cbsz:4 blgp:4
	v_mfma_f32_16x16x128_f8f6f4 v[62:65], v[156:159], v[66:69], v[2:5] cbsz:4 blgp:4
	v_mfma_f32_16x16x128_f8f6f4 v[58:61], v[168:171], v[70:73], v[58:61] cbsz:4 blgp:4
	v_mfma_f32_16x16x128_f8f6f4 v[62:65], v[172:175], v[70:73], v[62:65] cbsz:4 blgp:4
	v_mfma_f32_16x16x128_f8f6f4 v[66:69], v[142:145], v[74:77], v[6:9] cbsz:4 blgp:4
	v_mfma_f32_16x16x128_f8f6f4 v[70:73], v[156:159], v[74:77], v[2:5] cbsz:4 blgp:4
	v_mfma_f32_16x16x128_f8f6f4 v[66:69], v[168:171], v[78:81], v[66:69] cbsz:4 blgp:4
	v_mfma_f32_16x16x128_f8f6f4 v[70:73], v[172:175], v[78:81], v[70:73] cbsz:4 blgp:4
	v_mfma_f32_16x16x128_f8f6f4 v[74:77], v[142:145], v[86:89], v[6:9] cbsz:4 blgp:4
	v_mfma_f32_16x16x128_f8f6f4 v[78:81], v[156:159], v[86:89], v[2:5] cbsz:4 blgp:4
	v_mfma_f32_16x16x128_f8f6f4 v[74:77], v[168:171], v[90:93], v[74:77] cbsz:4 blgp:4
	v_mfma_f32_16x16x128_f8f6f4 v[78:81], v[172:175], v[90:93], v[78:81] cbsz:4 blgp:4
	s_setprio 0
	s_barrier
	ds_read_b128 v[114:117], v165 offset:16384
	ds_read_b128 v[122:125], v165 offset:18432
	ds_read_b128 v[130:133], v166 offset:16384
	ds_read_b128 v[134:137], v166 offset:18432
	ds_read_b128 v[176:179], v165 offset:20480
	ds_read_b128 v[180:183], v165 offset:22528
	ds_read_b128 v[184:187], v166 offset:20480
	ds_read_b128 v[188:191], v166 offset:22528
	s_mov_b32 m0, s55
	s_nop 0
	global_load_lds_dwordx4 v146, s[48:49]
	s_mov_b32 m0, s58
	s_nop 0
	global_load_lds_dwordx4 v150, s[48:49]
	s_barrier
	s_waitcnt lgkmcnt(0)
	s_setprio 1
	v_mfma_f32_16x16x128_f8f6f4 v[86:89], v[82:85], v[114:117], v[14:17] cbsz:4 blgp:4
	v_mfma_f32_16x16x128_f8f6f4 v[90:93], v[94:97], v[114:117], v[10:13] cbsz:4 blgp:4
	v_mfma_f32_16x16x128_f8f6f4 v[98:101], v[82:85], v[122:125], v[14:17] cbsz:4 blgp:4
	v_mfma_f32_16x16x128_f8f6f4 v[106:109], v[94:97], v[122:125], v[10:13] cbsz:4 blgp:4
	v_mfma_f32_16x16x128_f8f6f4 v[118:121], v[82:85], v[176:179], v[14:17] cbsz:4 blgp:4
	v_mfma_f32_16x16x128_f8f6f4 v[126:129], v[94:97], v[176:179], v[10:13] cbsz:4 blgp:4
	v_mfma_f32_16x16x128_f8f6f4 v[138:141], v[82:85], v[180:183], v[14:17] cbsz:4 blgp:4
	v_mfma_f32_16x16x128_f8f6f4 v[82:85], v[94:97], v[180:183], v[10:13] cbsz:4 blgp:4
	v_mfma_f32_16x16x128_f8f6f4 v[86:89], v[102:105], v[130:133], v[86:89] cbsz:4 blgp:4
	v_mfma_f32_16x16x128_f8f6f4 v[90:93], v[110:113], v[130:133], v[90:93] cbsz:4 blgp:4
	v_mfma_f32_16x16x128_f8f6f4 v[98:101], v[102:105], v[134:137], v[98:101] cbsz:4 blgp:4
	v_mfma_f32_16x16x128_f8f6f4 v[106:109], v[110:113], v[134:137], v[106:109] cbsz:4 blgp:4
	v_mfma_f32_16x16x128_f8f6f4 v[118:121], v[102:105], v[184:187], v[118:121] cbsz:4 blgp:4
	v_mfma_f32_16x16x128_f8f6f4 v[126:129], v[110:113], v[184:187], v[126:129] cbsz:4 blgp:4
	v_mfma_f32_16x16x128_f8f6f4 v[138:141], v[102:105], v[188:191], v[138:141] cbsz:4 blgp:4
	v_mfma_f32_16x16x128_f8f6f4 v[82:85], v[110:113], v[188:191], v[82:85] cbsz:4 blgp:4
	s_setprio 0
	s_barrier
	s_add_u32 s50, s50, s24
	s_addc_u32 s51, s51, s25
	s_mov_b32 m0, s59
	s_nop 0
	global_load_lds_dwordx4 v148, s[50:51]
	s_mov_b32 m0, s60
	s_nop 0
	global_load_lds_dwordx4 v152, s[50:51]
	s_waitcnt vmcnt(6)
	s_barrier
	s_setprio 1
	v_mfma_f32_16x16x128_f8f6f4 v[94:97], v[142:145], v[114:117], v[6:9] cbsz:4 blgp:4
	v_mfma_f32_16x16x128_f8f6f4 v[102:105], v[156:159], v[114:117], v[2:5] cbsz:4 blgp:4
	v_mfma_f32_16x16x128_f8f6f4 v[110:113], v[142:145], v[122:125], v[6:9] cbsz:4 blgp:4
	v_mfma_f32_16x16x128_f8f6f4 v[114:117], v[156:159], v[122:125], v[2:5] cbsz:4 blgp:4
	v_mfma_f32_16x16x128_f8f6f4 v[94:97], v[168:171], v[130:133], v[94:97] cbsz:4 blgp:4
	v_mfma_f32_16x16x128_f8f6f4 v[102:105], v[172:175], v[130:133], v[102:105] cbsz:4 blgp:4
	v_mfma_f32_16x16x128_f8f6f4 v[110:113], v[168:171], v[134:137], v[110:113] cbsz:4 blgp:4
	v_mfma_f32_16x16x128_f8f6f4 v[114:117], v[172:175], v[134:137], v[114:117] cbsz:4 blgp:4
	v_mfma_f32_16x16x128_f8f6f4 v[122:125], v[142:145], v[176:179], v[6:9] cbsz:4 blgp:4
	v_mfma_f32_16x16x128_f8f6f4 v[130:133], v[156:159], v[176:179], v[2:5] cbsz:4 blgp:4
	v_mfma_f32_16x16x128_f8f6f4 v[134:137], v[142:145], v[180:183], v[6:9] cbsz:4 blgp:4
	v_mfma_f32_16x16x128_f8f6f4 v[142:145], v[156:159], v[180:183], v[2:5] cbsz:4 blgp:4
	v_mfma_f32_16x16x128_f8f6f4 v[122:125], v[168:171], v[184:187], v[122:125] cbsz:4 blgp:4
	v_mfma_f32_16x16x128_f8f6f4 v[130:133], v[172:175], v[184:187], v[130:133] cbsz:4 blgp:4
	v_mfma_f32_16x16x128_f8f6f4 v[134:137], v[168:171], v[188:191], v[134:137] cbsz:4 blgp:4
	v_mfma_f32_16x16x128_f8f6f4 v[142:145], v[172:175], v[188:191], v[142:145] cbsz:4 blgp:4
	s_setprio 0
	s_barrier
	ds_read_b128 v[156:159], v163 offset:32768
	ds_read_b128 v[168:171], v163 offset:34816
	ds_read_b128 v[172:175], v164 offset:32768
	ds_read_b128 v[176:179], v164 offset:34816
	ds_read_b128 v[180:183], v165 offset:32768
	ds_read_b128 v[184:187], v165 offset:34816
	ds_read_b128 v[188:191], v166 offset:32768
	ds_read_b128 v[192:195], v166 offset:34816
	ds_read_b128 v[196:199], v165 offset:36864
	ds_read_b128 v[200:203], v165 offset:38912
	ds_read_b128 v[204:207], v166 offset:36864
	ds_read_b128 v[208:211], v166 offset:38912
	s_add_u32 s48, s48, s22
	s_addc_u32 s49, s49, s23
	s_mov_b32 m0, s61
	s_nop 0
	global_load_lds_dwordx4 v146, s[48:49]
	s_mov_b32 m0, s62
	s_nop 0
	global_load_lds_dwordx4 v150, s[48:49]
	s_waitcnt lgkmcnt(8)
	s_barrier
	s_waitcnt lgkmcnt(0)
	s_setprio 1
	v_mfma_f32_16x16x128_f8f6f4 v[18:21], v[156:159], v[180:183], v[18:21] cbsz:4 blgp:4
	v_mfma_f32_16x16x128_f8f6f4 v[22:25], v[168:171], v[180:183], v[22:25] cbsz:4 blgp:4
	v_mfma_f32_16x16x128_f8f6f4 v[26:29], v[156:159], v[184:187], v[26:29] cbsz:4 blgp:4
	v_mfma_f32_16x16x128_f8f6f4 v[30:33], v[168:171], v[184:187], v[30:33] cbsz:4 blgp:4
	v_mfma_f32_16x16x128_f8f6f4 v[34:37], v[156:159], v[196:199], v[34:37] cbsz:4 blgp:4
	v_mfma_f32_16x16x128_f8f6f4 v[38:41], v[168:171], v[196:199], v[38:41] cbsz:4 blgp:4
	v_mfma_f32_16x16x128_f8f6f4 v[42:45], v[156:159], v[200:203], v[42:45] cbsz:4 blgp:4
	v_mfma_f32_16x16x128_f8f6f4 v[46:49], v[168:171], v[200:203], v[46:49] cbsz:4 blgp:4
	v_mfma_f32_16x16x128_f8f6f4 v[18:21], v[172:175], v[188:191], v[18:21] cbsz:4 blgp:4
	v_mfma_f32_16x16x128_f8f6f4 v[22:25], v[176:179], v[188:191], v[22:25] cbsz:4 blgp:4
	v_mfma_f32_16x16x128_f8f6f4 v[26:29], v[172:175], v[192:195], v[26:29] cbsz:4 blgp:4
	v_mfma_f32_16x16x128_f8f6f4 v[30:33], v[176:179], v[192:195], v[30:33] cbsz:4 blgp:4
	v_mfma_f32_16x16x128_f8f6f4 v[34:37], v[172:175], v[204:207], v[34:37] cbsz:4 blgp:4
	v_mfma_f32_16x16x128_f8f6f4 v[38:41], v[176:179], v[204:207], v[38:41] cbsz:4 blgp:4
	v_mfma_f32_16x16x128_f8f6f4 v[42:45], v[172:175], v[208:211], v[42:45] cbsz:4 blgp:4
	v_mfma_f32_16x16x128_f8f6f4 v[46:49], v[176:179], v[208:211], v[46:49] cbsz:4 blgp:4
	s_setprio 0
	s_barrier
	ds_read_b128 v[212:215], v163 offset:49152
	ds_read_b128 v[216:219], v163 offset:51200
	ds_read_b128 v[220:223], v164 offset:49152
	ds_read_b128 v[224:227], v164 offset:51200
	s_mov_b32 m0, s65
	s_nop 0
	global_load_lds_dwordx4 v148, s[44:45]
	s_mov_b32 m0, s66
	s_nop 0
	global_load_lds_dwordx4 v152, s[44:45]
	s_barrier
	s_waitcnt lgkmcnt(0)
	s_setprio 1
	v_mfma_f32_16x16x128_f8f6f4 v[50:53], v[212:215], v[180:183], v[50:53] cbsz:4 blgp:4
	v_mfma_f32_16x16x128_f8f6f4 v[54:57], v[216:219], v[180:183], v[54:57] cbsz:4 blgp:4
	v_mfma_f32_16x16x128_f8f6f4 v[58:61], v[212:215], v[184:187], v[58:61] cbsz:4 blgp:4
	v_mfma_f32_16x16x128_f8f6f4 v[62:65], v[216:219], v[184:187], v[62:65] cbsz:4 blgp:4
	v_mfma_f32_16x16x128_f8f6f4 v[66:69], v[212:215], v[196:199], v[66:69] cbsz:4 blgp:4
	v_mfma_f32_16x16x128_f8f6f4 v[70:73], v[216:219], v[196:199], v[70:73] cbsz:4 blgp:4
	v_mfma_f32_16x16x128_f8f6f4 v[74:77], v[212:215], v[200:203], v[74:77] cbsz:4 blgp:4
	v_mfma_f32_16x16x128_f8f6f4 v[78:81], v[216:219], v[200:203], v[78:81] cbsz:4 blgp:4
	v_mfma_f32_16x16x128_f8f6f4 v[50:53], v[220:223], v[188:191], v[50:53] cbsz:4 blgp:4
	v_mfma_f32_16x16x128_f8f6f4 v[54:57], v[224:227], v[188:191], v[54:57] cbsz:4 blgp:4
	v_mfma_f32_16x16x128_f8f6f4 v[58:61], v[220:223], v[192:195], v[58:61] cbsz:4 blgp:4
	v_mfma_f32_16x16x128_f8f6f4 v[62:65], v[224:227], v[192:195], v[62:65] cbsz:4 blgp:4
	v_mfma_f32_16x16x128_f8f6f4 v[66:69], v[220:223], v[204:207], v[66:69] cbsz:4 blgp:4
	v_mfma_f32_16x16x128_f8f6f4 v[70:73], v[224:227], v[204:207], v[70:73] cbsz:4 blgp:4
	v_mfma_f32_16x16x128_f8f6f4 v[74:77], v[220:223], v[208:211], v[74:77] cbsz:4 blgp:4
	v_mfma_f32_16x16x128_f8f6f4 v[78:81], v[224:227], v[208:211], v[78:81] cbsz:4 blgp:4
	s_setprio 0
	s_barrier
	ds_read_b128 v[180:183], v165 offset:49152
	ds_read_b128 v[184:187], v165 offset:51200
	ds_read_b128 v[188:191], v166 offset:49152
	ds_read_b128 v[192:195], v166 offset:51200
	ds_read_b128 v[196:199], v165 offset:53248
	ds_read_b128 v[200:203], v165 offset:55296
	ds_read_b128 v[204:207], v166 offset:53248
	ds_read_b128 v[208:211], v166 offset:55296
	s_mov_b32 m0, s67
	s_nop 0
	global_load_lds_dwordx4 v146, s[46:47]
	s_mov_b32 m0, s68
	s_nop 0
	global_load_lds_dwordx4 v150, s[46:47]
	s_barrier
	s_waitcnt lgkmcnt(0)
	s_setprio 1
	v_mfma_f32_16x16x128_f8f6f4 v[86:89], v[156:159], v[180:183], v[86:89] cbsz:4 blgp:4
	v_mfma_f32_16x16x128_f8f6f4 v[90:93], v[168:171], v[180:183], v[90:93] cbsz:4 blgp:4
	v_mfma_f32_16x16x128_f8f6f4 v[98:101], v[156:159], v[184:187], v[98:101] cbsz:4 blgp:4
	v_mfma_f32_16x16x128_f8f6f4 v[106:109], v[168:171], v[184:187], v[106:109] cbsz:4 blgp:4
	v_mfma_f32_16x16x128_f8f6f4 v[118:121], v[156:159], v[196:199], v[118:121] cbsz:4 blgp:4
	v_mfma_f32_16x16x128_f8f6f4 v[126:129], v[168:171], v[196:199], v[126:129] cbsz:4 blgp:4
	v_mfma_f32_16x16x128_f8f6f4 v[138:141], v[156:159], v[200:203], v[138:141] cbsz:4 blgp:4
	v_mfma_f32_16x16x128_f8f6f4 v[82:85], v[168:171], v[200:203], v[82:85] cbsz:4 blgp:4
	v_mfma_f32_16x16x128_f8f6f4 v[86:89], v[172:175], v[188:191], v[86:89] cbsz:4 blgp:4
	v_mfma_f32_16x16x128_f8f6f4 v[90:93], v[176:179], v[188:191], v[90:93] cbsz:4 blgp:4
	v_mfma_f32_16x16x128_f8f6f4 v[98:101], v[172:175], v[192:195], v[98:101] cbsz:4 blgp:4
	v_mfma_f32_16x16x128_f8f6f4 v[106:109], v[176:179], v[192:195], v[106:109] cbsz:4 blgp:4
	v_mfma_f32_16x16x128_f8f6f4 v[118:121], v[172:175], v[204:207], v[118:121] cbsz:4 blgp:4
	v_mfma_f32_16x16x128_f8f6f4 v[126:129], v[176:179], v[204:207], v[126:129] cbsz:4 blgp:4
	v_mfma_f32_16x16x128_f8f6f4 v[138:141], v[172:175], v[208:211], v[138:141] cbsz:4 blgp:4
	v_mfma_f32_16x16x128_f8f6f4 v[82:85], v[176:179], v[208:211], v[82:85] cbsz:4 blgp:4
	s_setprio 0
	s_barrier
	s_add_u32 s44, s44, s24
	s_addc_u32 s45, s45, s25
	s_mov_b32 m0, s69
	s_nop 0
	global_load_lds_dwordx4 v148, s[44:45]
	s_mov_b32 m0, s70
	s_nop 0
	global_load_lds_dwordx4 v152, s[44:45]
	s_waitcnt vmcnt(6)
	s_barrier
	s_setprio 1
	v_mfma_f32_16x16x128_f8f6f4 v[94:97], v[212:215], v[180:183], v[94:97] cbsz:4 blgp:4
	v_mfma_f32_16x16x128_f8f6f4 v[102:105], v[216:219], v[180:183], v[102:105] cbsz:4 blgp:4
	v_mfma_f32_16x16x128_f8f6f4 v[110:113], v[212:215], v[184:187], v[110:113] cbsz:4 blgp:4
	v_mfma_f32_16x16x128_f8f6f4 v[114:117], v[216:219], v[184:187], v[114:117] cbsz:4 blgp:4
	v_mfma_f32_16x16x128_f8f6f4 v[122:125], v[212:215], v[196:199], v[122:125] cbsz:4 blgp:4
	v_mfma_f32_16x16x128_f8f6f4 v[130:133], v[216:219], v[196:199], v[130:133] cbsz:4 blgp:4
	v_mfma_f32_16x16x128_f8f6f4 v[134:137], v[212:215], v[200:203], v[134:137] cbsz:4 blgp:4
	v_mfma_f32_16x16x128_f8f6f4 v[142:145], v[216:219], v[200:203], v[142:145] cbsz:4 blgp:4
	v_mfma_f32_16x16x128_f8f6f4 v[94:97], v[220:223], v[188:191], v[94:97] cbsz:4 blgp:4
	v_mfma_f32_16x16x128_f8f6f4 v[102:105], v[224:227], v[188:191], v[102:105] cbsz:4 blgp:4
	v_mfma_f32_16x16x128_f8f6f4 v[110:113], v[220:223], v[192:195], v[110:113] cbsz:4 blgp:4
	v_mfma_f32_16x16x128_f8f6f4 v[114:117], v[224:227], v[192:195], v[114:117] cbsz:4 blgp:4
	v_mfma_f32_16x16x128_f8f6f4 v[122:125], v[220:223], v[204:207], v[122:125] cbsz:4 blgp:4
	v_mfma_f32_16x16x128_f8f6f4 v[130:133], v[224:227], v[204:207], v[130:133] cbsz:4 blgp:4
	v_mfma_f32_16x16x128_f8f6f4 v[134:137], v[220:223], v[208:211], v[134:137] cbsz:4 blgp:4
	v_mfma_f32_16x16x128_f8f6f4 v[142:145], v[224:227], v[208:211], v[142:145] cbsz:4 blgp:4
	s_setprio 0
	s_andn2_b64 vcc, exec, s[34:35]
	s_barrier
	s_cbranch_vccnz .LBB5_4
	s_ashr_i32 s29, s28, 31
	s_lshl_b64 s[44:45], s[28:29], 10
	s_add_u32 s44, s10, s44
	s_addc_u32 s45, s11, s45
	s_add_u32 s29, s42, 0x200
	s_addc_u32 s79, s43, 0
	s_add_u32 s80, s40, 0x200
	s_addc_u32 s81, s41, 0
	s_add_u32 s40, s82, 0x180
	s_addc_u32 s41, s83, 0
	s_mov_b32 s82, 4
	s_cmp_eq_u32 s64, s82
	s_cselect_b64 s[42:43], -1, 0
	s_cmp_lg_u32 s64, s82
	s_cbranch_scc1 .LBB5_15

.LBB5_15:
	ds_read_b128 v[156:159], v163
	ds_read_b128 v[168:171], v163 offset:2048
	ds_read_b128 v[172:175], v164
	ds_read_b128 v[176:179], v164 offset:2048
	s_and_b64 s[42:43], s[42:43], exec
	s_cselect_b32 s48, s38, s29
	s_cselect_b32 s49, s39, s79
	s_cselect_b32 s51, s5, s81
	s_cselect_b32 s50, s4, s80
	s_add_u32 s46, s48, 0x80
	s_addc_u32 s47, s49, 0
	s_add_u32 s42, s50, 0x80
	s_addc_u32 s43, s51, 0
	ds_read_b128 v[180:183], v165
	ds_read_b128 v[184:187], v165 offset:2048
	ds_read_b128 v[188:191], v166
	ds_read_b128 v[192:195], v166 offset:2048
	ds_read_b128 v[196:199], v165 offset:4096
	ds_read_b128 v[200:203], v165 offset:6144
	ds_read_b128 v[204:207], v166 offset:4096
	ds_read_b128 v[208:211], v166 offset:6144
	s_mov_b32 m0, s71
	s_nop 0
	global_load_lds_dwordx4 v146, s[40:41]
	s_mov_b32 m0, s72
	s_nop 0
	global_load_lds_dwordx4 v150, s[40:41]
	s_waitcnt lgkmcnt(8)
	s_barrier
	s_waitcnt lgkmcnt(0)
	s_setprio 1
	v_mfma_f32_16x16x128_f8f6f4 v[18:21], v[156:159], v[180:183], v[18:21] cbsz:4 blgp:4
	v_mfma_f32_16x16x128_f8f6f4 v[22:25], v[168:171], v[180:183], v[22:25] cbsz:4 blgp:4
	v_mfma_f32_16x16x128_f8f6f4 v[26:29], v[156:159], v[184:187], v[26:29] cbsz:4 blgp:4
	v_mfma_f32_16x16x128_f8f6f4 v[30:33], v[168:171], v[184:187], v[30:33] cbsz:4 blgp:4
	v_mfma_f32_16x16x128_f8f6f4 v[34:37], v[156:159], v[196:199], v[34:37] cbsz:4 blgp:4
	v_mfma_f32_16x16x128_f8f6f4 v[38:41], v[168:171], v[196:199], v[38:41] cbsz:4 blgp:4
	v_mfma_f32_16x16x128_f8f6f4 v[42:45], v[156:159], v[200:203], v[42:45] cbsz:4 blgp:4
	v_mfma_f32_16x16x128_f8f6f4 v[46:49], v[168:171], v[200:203], v[46:49] cbsz:4 blgp:4
	v_mfma_f32_16x16x128_f8f6f4 v[18:21], v[172:175], v[188:191], v[18:21] cbsz:4 blgp:4
	v_mfma_f32_16x16x128_f8f6f4 v[22:25], v[176:179], v[188:191], v[22:25] cbsz:4 blgp:4
	v_mfma_f32_16x16x128_f8f6f4 v[26:29], v[172:175], v[192:195], v[26:29] cbsz:4 blgp:4
	v_mfma_f32_16x16x128_f8f6f4 v[30:33], v[176:179], v[192:195], v[30:33] cbsz:4 blgp:4
	v_mfma_f32_16x16x128_f8f6f4 v[34:37], v[172:175], v[204:207], v[34:37] cbsz:4 blgp:4
	v_mfma_f32_16x16x128_f8f6f4 v[38:41], v[176:179], v[204:207], v[38:41] cbsz:4 blgp:4
	v_mfma_f32_16x16x128_f8f6f4 v[42:45], v[172:175], v[208:211], v[42:45] cbsz:4 blgp:4
	v_mfma_f32_16x16x128_f8f6f4 v[46:49], v[176:179], v[208:211], v[46:49] cbsz:4 blgp:4
	s_setprio 0
	s_barrier
	ds_read_b128 v[212:215], v163 offset:16384
	ds_read_b128 v[216:219], v163 offset:18432
	ds_read_b128 v[220:223], v164 offset:16384
	ds_read_b128 v[224:227], v164 offset:18432
	s_mov_b32 m0, s56
	s_nop 0
	global_load_lds_dwordx4 v148, s[50:51]
	s_mov_b32 m0, s57
	s_nop 0
	global_load_lds_dwordx4 v152, s[50:51]
	s_barrier
	s_waitcnt lgkmcnt(0)
	s_setprio 1
	v_mfma_f32_16x16x128_f8f6f4 v[50:53], v[212:215], v[180:183], v[50:53] cbsz:4 blgp:4
	v_mfma_f32_16x16x128_f8f6f4 v[54:57], v[216:219], v[180:183], v[54:57] cbsz:4 blgp:4
	v_mfma_f32_16x16x128_f8f6f4 v[58:61], v[212:215], v[184:187], v[58:61] cbsz:4 blgp:4
	v_mfma_f32_16x16x128_f8f6f4 v[62:65], v[216:219], v[184:187], v[62:65] cbsz:4 blgp:4
	v_mfma_f32_16x16x128_f8f6f4 v[66:69], v[212:215], v[196:199], v[66:69] cbsz:4 blgp:4
	v_mfma_f32_16x16x128_f8f6f4 v[70:73], v[216:219], v[196:199], v[70:73] cbsz:4 blgp:4
	v_mfma_f32_16x16x128_f8f6f4 v[74:77], v[212:215], v[200:203], v[74:77] cbsz:4 blgp:4
	v_mfma_f32_16x16x128_f8f6f4 v[78:81], v[216:219], v[200:203], v[78:81] cbsz:4 blgp:4
	v_mfma_f32_16x16x128_f8f6f4 v[50:53], v[220:223], v[188:191], v[50:53] cbsz:4 blgp:4
	v_mfma_f32_16x16x128_f8f6f4 v[54:57], v[224:227], v[188:191], v[54:57] cbsz:4 blgp:4
	v_mfma_f32_16x16x128_f8f6f4 v[58:61], v[220:223], v[192:195], v[58:61] cbsz:4 blgp:4
	v_mfma_f32_16x16x128_f8f6f4 v[62:65], v[224:227], v[192:195], v[62:65] cbsz:4 blgp:4
	v_mfma_f32_16x16x128_f8f6f4 v[66:69], v[220:223], v[204:207], v[66:69] cbsz:4 blgp:4
	v_mfma_f32_16x16x128_f8f6f4 v[70:73], v[224:227], v[204:207], v[70:73] cbsz:4 blgp:4
	v_mfma_f32_16x16x128_f8f6f4 v[74:77], v[220:223], v[208:211], v[74:77] cbsz:4 blgp:4
	v_mfma_f32_16x16x128_f8f6f4 v[78:81], v[224:227], v[208:211], v[78:81] cbsz:4 blgp:4
	s_setprio 0
	s_barrier
	ds_read_b128 v[180:183], v165 offset:16384
	ds_read_b128 v[184:187], v165 offset:18432
	ds_read_b128 v[188:191], v166 offset:16384
	ds_read_b128 v[192:195], v166 offset:18432
	ds_read_b128 v[196:199], v165 offset:20480
	ds_read_b128 v[200:203], v165 offset:22528
	ds_read_b128 v[204:207], v166 offset:20480
	ds_read_b128 v[208:211], v166 offset:22528
	s_mov_b32 m0, s55
	s_nop 0
	global_load_lds_dwordx4 v146, s[48:49]
	s_mov_b32 m0, s58
	s_nop 0
	global_load_lds_dwordx4 v150, s[48:49]
	s_barrier
	s_waitcnt lgkmcnt(0)
	s_setprio 1
	v_mfma_f32_16x16x128_f8f6f4 v[86:89], v[156:159], v[180:183], v[86:89] cbsz:4 blgp:4
	v_mfma_f32_16x16x128_f8f6f4 v[90:93], v[168:171], v[180:183], v[90:93] cbsz:4 blgp:4
	v_mfma_f32_16x16x128_f8f6f4 v[98:101], v[156:159], v[184:187], v[98:101] cbsz:4 blgp:4
	v_mfma_f32_16x16x128_f8f6f4 v[106:109], v[168:171], v[184:187], v[106:109] cbsz:4 blgp:4
	v_mfma_f32_16x16x128_f8f6f4 v[118:121], v[156:159], v[196:199], v[118:121] cbsz:4 blgp:4
	v_mfma_f32_16x16x128_f8f6f4 v[126:129], v[168:171], v[196:199], v[126:129] cbsz:4 blgp:4
	v_mfma_f32_16x16x128_f8f6f4 v[138:141], v[156:159], v[200:203], v[138:141] cbsz:4 blgp:4
	v_mfma_f32_16x16x128_f8f6f4 v[82:85], v[168:171], v[200:203], v[82:85] cbsz:4 blgp:4
	v_mfma_f32_16x16x128_f8f6f4 v[86:89], v[172:175], v[188:191], v[86:89] cbsz:4 blgp:4
	v_mfma_f32_16x16x128_f8f6f4 v[90:93], v[176:179], v[188:191], v[90:93] cbsz:4 blgp:4
	v_mfma_f32_16x16x128_f8f6f4 v[98:101], v[172:175], v[192:195], v[98:101] cbsz:4 blgp:4
	v_mfma_f32_16x16x128_f8f6f4 v[106:109], v[176:179], v[192:195], v[106:109] cbsz:4 blgp:4
	v_mfma_f32_16x16x128_f8f6f4 v[118:121], v[172:175], v[204:207], v[118:121] cbsz:4 blgp:4
	v_mfma_f32_16x16x128_f8f6f4 v[126:129], v[176:179], v[204:207], v[126:129] cbsz:4 blgp:4
	v_mfma_f32_16x16x128_f8f6f4 v[138:141], v[172:175], v[208:211], v[138:141] cbsz:4 blgp:4
	v_mfma_f32_16x16x128_f8f6f4 v[82:85], v[176:179], v[208:211], v[82:85] cbsz:4 blgp:4
	s_setprio 0
	s_barrier
	s_add_u32 s50, s50, s24
	s_addc_u32 s51, s51, s25
	s_mov_b32 m0, s59
	s_nop 0
	global_load_lds_dwordx4 v148, s[50:51]
	s_mov_b32 m0, s60
	s_nop 0
	global_load_lds_dwordx4 v152, s[50:51]
	s_waitcnt vmcnt(6)
	s_barrier
	s_setprio 1
	v_mfma_f32_16x16x128_f8f6f4 v[94:97], v[212:215], v[180:183], v[94:97] cbsz:4 blgp:4
	v_mfma_f32_16x16x128_f8f6f4 v[102:105], v[216:219], v[180:183], v[102:105] cbsz:4 blgp:4
	v_mfma_f32_16x16x128_f8f6f4 v[110:113], v[212:215], v[184:187], v[110:113] cbsz:4 blgp:4
	v_mfma_f32_16x16x128_f8f6f4 v[114:117], v[216:219], v[184:187], v[114:117] cbsz:4 blgp:4
	v_mfma_f32_16x16x128_f8f6f4 v[122:125], v[212:215], v[196:199], v[122:125] cbsz:4 blgp:4
	v_mfma_f32_16x16x128_f8f6f4 v[130:133], v[216:219], v[196:199], v[130:133] cbsz:4 blgp:4
	v_mfma_f32_16x16x128_f8f6f4 v[134:137], v[212:215], v[200:203], v[134:137] cbsz:4 blgp:4
	v_mfma_f32_16x16x128_f8f6f4 v[142:145], v[216:219], v[200:203], v[142:145] cbsz:4 blgp:4
	v_mfma_f32_16x16x128_f8f6f4 v[94:97], v[220:223], v[188:191], v[94:97] cbsz:4 blgp:4
	v_mfma_f32_16x16x128_f8f6f4 v[102:105], v[224:227], v[188:191], v[102:105] cbsz:4 blgp:4
	v_mfma_f32_16x16x128_f8f6f4 v[110:113], v[220:223], v[192:195], v[110:113] cbsz:4 blgp:4
	v_mfma_f32_16x16x128_f8f6f4 v[114:117], v[224:227], v[192:195], v[114:117] cbsz:4 blgp:4
	v_mfma_f32_16x16x128_f8f6f4 v[122:125], v[220:223], v[204:207], v[122:125] cbsz:4 blgp:4
	v_mfma_f32_16x16x128_f8f6f4 v[130:133], v[224:227], v[204:207], v[130:133] cbsz:4 blgp:4
	v_mfma_f32_16x16x128_f8f6f4 v[134:137], v[220:223], v[208:211], v[134:137] cbsz:4 blgp:4
	v_mfma_f32_16x16x128_f8f6f4 v[142:145], v[224:227], v[208:211], v[142:145] cbsz:4 blgp:4
	s_setprio 0
	s_barrier
	ds_read_b128 v[156:159], v163 offset:32768
	ds_read_b128 v[168:171], v163 offset:34816
	ds_read_b128 v[172:175], v164 offset:32768
	ds_read_b128 v[176:179], v164 offset:34816
	ds_read_b128 v[180:183], v165 offset:32768
	ds_read_b128 v[184:187], v165 offset:34816
	ds_read_b128 v[188:191], v166 offset:32768
	ds_read_b128 v[192:195], v166 offset:34816
	ds_read_b128 v[196:199], v165 offset:36864
	ds_read_b128 v[200:203], v165 offset:38912
	ds_read_b128 v[204:207], v166 offset:36864
	ds_read_b128 v[208:211], v166 offset:38912
	s_add_u32 s48, s48, s22
	s_addc_u32 s49, s49, s23
	s_mov_b32 m0, s61
	s_nop 0
	global_load_lds_dwordx4 v146, s[48:49]
	s_mov_b32 m0, s62
	s_nop 0
	global_load_lds_dwordx4 v150, s[48:49]
	s_waitcnt lgkmcnt(8)
	s_barrier
	s_waitcnt lgkmcnt(0)
	s_setprio 1
	v_mfma_f32_16x16x128_f8f6f4 v[18:21], v[156:159], v[180:183], v[18:21] cbsz:4 blgp:4
	v_mfma_f32_16x16x128_f8f6f4 v[22:25], v[168:171], v[180:183], v[22:25] cbsz:4 blgp:4
	v_mfma_f32_16x16x128_f8f6f4 v[26:29], v[156:159], v[184:187], v[26:29] cbsz:4 blgp:4
	v_mfma_f32_16x16x128_f8f6f4 v[30:33], v[168:171], v[184:187], v[30:33] cbsz:4 blgp:4
	v_mfma_f32_16x16x128_f8f6f4 v[34:37], v[156:159], v[196:199], v[34:37] cbsz:4 blgp:4
	v_mfma_f32_16x16x128_f8f6f4 v[38:41], v[168:171], v[196:199], v[38:41] cbsz:4 blgp:4
	v_mfma_f32_16x16x128_f8f6f4 v[42:45], v[156:159], v[200:203], v[42:45] cbsz:4 blgp:4
	v_mfma_f32_16x16x128_f8f6f4 v[46:49], v[168:171], v[200:203], v[46:49] cbsz:4 blgp:4
	v_mfma_f32_16x16x128_f8f6f4 v[18:21], v[172:175], v[188:191], v[18:21] cbsz:4 blgp:4
	v_mfma_f32_16x16x128_f8f6f4 v[22:25], v[176:179], v[188:191], v[22:25] cbsz:4 blgp:4
	v_mfma_f32_16x16x128_f8f6f4 v[26:29], v[172:175], v[192:195], v[26:29] cbsz:4 blgp:4
	v_mfma_f32_16x16x128_f8f6f4 v[30:33], v[176:179], v[192:195], v[30:33] cbsz:4 blgp:4
	v_mfma_f32_16x16x128_f8f6f4 v[34:37], v[172:175], v[204:207], v[34:37] cbsz:4 blgp:4
	v_mfma_f32_16x16x128_f8f6f4 v[38:41], v[176:179], v[204:207], v[38:41] cbsz:4 blgp:4
	v_mfma_f32_16x16x128_f8f6f4 v[42:45], v[172:175], v[208:211], v[42:45] cbsz:4 blgp:4
	v_mfma_f32_16x16x128_f8f6f4 v[46:49], v[176:179], v[208:211], v[46:49] cbsz:4 blgp:4
	s_setprio 0
	s_barrier
	ds_read_b128 v[212:215], v163 offset:49152
	ds_read_b128 v[216:219], v163 offset:51200
	ds_read_b128 v[220:223], v164 offset:49152
	ds_read_b128 v[224:227], v164 offset:51200
	s_mov_b32 m0, s65
	s_nop 0
	global_load_lds_dwordx4 v148, s[42:43]
	s_mov_b32 m0, s66
	s_nop 0
	global_load_lds_dwordx4 v152, s[42:43]
	s_barrier
	s_waitcnt lgkmcnt(0)
	s_setprio 1
	v_mfma_f32_16x16x128_f8f6f4 v[50:53], v[212:215], v[180:183], v[50:53] cbsz:4 blgp:4
	v_mfma_f32_16x16x128_f8f6f4 v[54:57], v[216:219], v[180:183], v[54:57] cbsz:4 blgp:4
	v_mfma_f32_16x16x128_f8f6f4 v[58:61], v[212:215], v[184:187], v[58:61] cbsz:4 blgp:4
	v_mfma_f32_16x16x128_f8f6f4 v[62:65], v[216:219], v[184:187], v[62:65] cbsz:4 blgp:4
	v_mfma_f32_16x16x128_f8f6f4 v[66:69], v[212:215], v[196:199], v[66:69] cbsz:4 blgp:4
	v_mfma_f32_16x16x128_f8f6f4 v[70:73], v[216:219], v[196:199], v[70:73] cbsz:4 blgp:4
	v_mfma_f32_16x16x128_f8f6f4 v[74:77], v[212:215], v[200:203], v[74:77] cbsz:4 blgp:4
	v_mfma_f32_16x16x128_f8f6f4 v[78:81], v[216:219], v[200:203], v[78:81] cbsz:4 blgp:4
	v_mfma_f32_16x16x128_f8f6f4 v[50:53], v[220:223], v[188:191], v[50:53] cbsz:4 blgp:4
	v_mfma_f32_16x16x128_f8f6f4 v[54:57], v[224:227], v[188:191], v[54:57] cbsz:4 blgp:4
	v_mfma_f32_16x16x128_f8f6f4 v[58:61], v[220:223], v[192:195], v[58:61] cbsz:4 blgp:4
	v_mfma_f32_16x16x128_f8f6f4 v[62:65], v[224:227], v[192:195], v[62:65] cbsz:4 blgp:4
	v_mfma_f32_16x16x128_f8f6f4 v[66:69], v[220:223], v[204:207], v[66:69] cbsz:4 blgp:4
	v_mfma_f32_16x16x128_f8f6f4 v[70:73], v[224:227], v[204:207], v[70:73] cbsz:4 blgp:4
	v_mfma_f32_16x16x128_f8f6f4 v[74:77], v[220:223], v[208:211], v[74:77] cbsz:4 blgp:4
	v_mfma_f32_16x16x128_f8f6f4 v[78:81], v[224:227], v[208:211], v[78:81] cbsz:4 blgp:4
	s_setprio 0
	s_barrier
	ds_read_b128 v[180:183], v165 offset:49152
	ds_read_b128 v[184:187], v165 offset:51200
	ds_read_b128 v[188:191], v166 offset:49152
	ds_read_b128 v[192:195], v166 offset:51200
	ds_read_b128 v[196:199], v165 offset:53248
	ds_read_b128 v[200:203], v165 offset:55296
	ds_read_b128 v[204:207], v166 offset:53248
	ds_read_b128 v[208:211], v166 offset:55296
	s_mov_b32 m0, s67
	s_nop 0
	global_load_lds_dwordx4 v146, s[46:47]
	s_mov_b32 m0, s68
	s_nop 0
	global_load_lds_dwordx4 v150, s[46:47]
	s_barrier
	s_waitcnt lgkmcnt(0)
	s_setprio 1
	v_mfma_f32_16x16x128_f8f6f4 v[86:89], v[156:159], v[180:183], v[86:89] cbsz:4 blgp:4
	v_mfma_f32_16x16x128_f8f6f4 v[90:93], v[168:171], v[180:183], v[90:93] cbsz:4 blgp:4
	v_mfma_f32_16x16x128_f8f6f4 v[98:101], v[156:159], v[184:187], v[98:101] cbsz:4 blgp:4
	v_mfma_f32_16x16x128_f8f6f4 v[106:109], v[168:171], v[184:187], v[106:109] cbsz:4 blgp:4
	v_mfma_f32_16x16x128_f8f6f4 v[118:121], v[156:159], v[196:199], v[118:121] cbsz:4 blgp:4
	v_mfma_f32_16x16x128_f8f6f4 v[126:129], v[168:171], v[196:199], v[126:129] cbsz:4 blgp:4
	v_mfma_f32_16x16x128_f8f6f4 v[138:141], v[156:159], v[200:203], v[138:141] cbsz:4 blgp:4
	v_mfma_f32_16x16x128_f8f6f4 v[82:85], v[168:171], v[200:203], v[82:85] cbsz:4 blgp:4
	v_mfma_f32_16x16x128_f8f6f4 v[86:89], v[172:175], v[188:191], v[86:89] cbsz:4 blgp:4
	v_mfma_f32_16x16x128_f8f6f4 v[90:93], v[176:179], v[188:191], v[90:93] cbsz:4 blgp:4
	v_mfma_f32_16x16x128_f8f6f4 v[98:101], v[172:175], v[192:195], v[98:101] cbsz:4 blgp:4
	v_mfma_f32_16x16x128_f8f6f4 v[106:109], v[176:179], v[192:195], v[106:109] cbsz:4 blgp:4
	v_mfma_f32_16x16x128_f8f6f4 v[118:121], v[172:175], v[204:207], v[118:121] cbsz:4 blgp:4
	v_mfma_f32_16x16x128_f8f6f4 v[126:129], v[176:179], v[204:207], v[126:129] cbsz:4 blgp:4
	v_mfma_f32_16x16x128_f8f6f4 v[138:141], v[172:175], v[208:211], v[138:141] cbsz:4 blgp:4
	v_mfma_f32_16x16x128_f8f6f4 v[82:85], v[176:179], v[208:211], v[82:85] cbsz:4 blgp:4
	s_setprio 0
	s_barrier
	s_add_u32 s42, s42, s24
	s_addc_u32 s43, s43, s25
	s_mov_b32 m0, s69
	s_nop 0
	global_load_lds_dwordx4 v148, s[42:43]
	s_mov_b32 m0, s70
	s_nop 0
	global_load_lds_dwordx4 v152, s[42:43]
	s_waitcnt vmcnt(6)
	s_barrier
	s_setprio 1
	v_mfma_f32_16x16x128_f8f6f4 v[94:97], v[212:215], v[180:183], v[94:97] cbsz:4 blgp:4
	v_mfma_f32_16x16x128_f8f6f4 v[102:105], v[216:219], v[180:183], v[102:105] cbsz:4 blgp:4
	v_mfma_f32_16x16x128_f8f6f4 v[110:113], v[212:215], v[184:187], v[110:113] cbsz:4 blgp:4
	v_mfma_f32_16x16x128_f8f6f4 v[114:117], v[216:219], v[184:187], v[114:117] cbsz:4 blgp:4
	v_mfma_f32_16x16x128_f8f6f4 v[122:125], v[212:215], v[196:199], v[122:125] cbsz:4 blgp:4
	v_mfma_f32_16x16x128_f8f6f4 v[130:133], v[216:219], v[196:199], v[130:133] cbsz:4 blgp:4
	v_mfma_f32_16x16x128_f8f6f4 v[134:137], v[212:215], v[200:203], v[134:137] cbsz:4 blgp:4
	v_mfma_f32_16x16x128_f8f6f4 v[142:145], v[216:219], v[200:203], v[142:145] cbsz:4 blgp:4
	v_mfma_f32_16x16x128_f8f6f4 v[94:97], v[220:223], v[188:191], v[94:97] cbsz:4 blgp:4
	v_mfma_f32_16x16x128_f8f6f4 v[102:105], v[224:227], v[188:191], v[102:105] cbsz:4 blgp:4
	v_mfma_f32_16x16x128_f8f6f4 v[110:113], v[220:223], v[192:195], v[110:113] cbsz:4 blgp:4
	v_mfma_f32_16x16x128_f8f6f4 v[114:117], v[224:227], v[192:195], v[114:117] cbsz:4 blgp:4
	v_mfma_f32_16x16x128_f8f6f4 v[122:125], v[220:223], v[204:207], v[122:125] cbsz:4 blgp:4
	v_mfma_f32_16x16x128_f8f6f4 v[130:133], v[224:227], v[204:207], v[130:133] cbsz:4 blgp:4
	v_mfma_f32_16x16x128_f8f6f4 v[134:137], v[220:223], v[208:211], v[134:137] cbsz:4 blgp:4
	v_mfma_f32_16x16x128_f8f6f4 v[142:145], v[224:227], v[208:211], v[142:145] cbsz:4 blgp:4
	s_setprio 0
	s_add_i32 s42, s82, 2
	s_add_u32 s29, s29, 0x100
	s_addc_u32 s79, s79, 0
	s_add_u32 s80, s80, 0x100
	s_addc_u32 s81, s81, 0
	s_add_u32 s40, s40, 0x100
	s_addc_u32 s41, s41, 0
	s_cmp_ge_i32 s82, s64
	s_barrier
	s_cbranch_scc1 .LBB5_4
	s_mov_b32 s82, s42
	s_cmp_eq_u32 s64, s82
	s_cselect_b64 s[42:43], -1, 0
	s_cmp_lg_u32 s64, s82
	s_cbranch_scc0 .LBB5_14
	s_branch .LBB5_15

.LBB6_15:
	s_add_u32 s82, s36, s20
	s_addc_u32 s83, s37, s21
	s_add_u32 s31, s36, 0x100
	s_addc_u32 s39, s37, 0
	s_and_b64 s[40:41], s[12:13], exec
	ds_read_b128 v[82:85], v169
	ds_read_b128 v[94:97], v169 offset:2048
	ds_read_b128 v[102:105], v178
	ds_read_b128 v[110:113], v178 offset:2048
	s_cselect_b32 s45, s5, s39
	s_cselect_b32 s44, s4, s31
	s_add_u32 s31, s34, 0x100
	s_addc_u32 s39, s35, 0
	s_and_b64 s[40:41], s[12:13], exec
	s_cselect_b32 s47, s7, s39
	s_cselect_b32 s46, s6, s31
	s_add_u32 s42, s44, 0x80
	s_addc_u32 s43, s45, 0
	s_add_u32 s40, s46, 0x80
	s_addc_u32 s41, s47, 0
	ds_read_b128 v[58:61], v179
	ds_read_b128 v[66:69], v179 offset:2048
	ds_read_b128 v[62:65], v180
	ds_read_b128 v[70:73], v180 offset:2048
	ds_read_b128 v[74:77], v179 offset:4096
	ds_read_b128 v[86:89], v179 offset:6144
	ds_read_b128 v[78:81], v180 offset:4096
	ds_read_b128 v[90:93], v180 offset:6144
	s_add_u32 s84, s82, 0x80
	s_addc_u32 s85, s83, 0
	s_mov_b32 m0, s68
	s_nop 0
	global_load_lds_dwordx4 v162, s[84:85]
	s_mov_b32 m0, s69
	s_nop 0
	global_load_lds_dwordx4 v166, s[84:85]
	s_waitcnt lgkmcnt(8)
	s_barrier
	s_waitcnt lgkmcnt(0)
	s_waitcnt vmcnt(16)
	v_mov_b32_e32 v171, v170
	v_pk_mul_f32 v[16:17], v[170:171], v[16:17]
	v_pk_mul_f32 v[14:15], v[172:173], v[14:15]
	v_pk_mul_f32 v[12:13], v[170:171], v[12:13]
	v_pk_mul_f32 v[10:11], v[172:173], v[10:11]
	v_pk_mul_f32 v[8:9], v[170:171], v[8:9]
	v_pk_mul_f32 v[6:7], v[172:173], v[6:7]
	v_pk_mul_f32 v[4:5], v[170:171], v[4:5]
	v_pk_mul_f32 v[2:3], v[172:173], v[2:3]
	s_setprio 1
	v_mfma_f32_16x16x128_f8f6f4 v[18:21], v[82:85], v[58:61], v[14:17] cbsz:4 blgp:4
	v_mfma_f32_16x16x128_f8f6f4 v[22:25], v[94:97], v[58:61], v[10:13] cbsz:4 blgp:4
	v_mfma_f32_16x16x128_f8f6f4 v[26:29], v[82:85], v[66:69], v[14:17] cbsz:4 blgp:4
	v_mfma_f32_16x16x128_f8f6f4 v[30:33], v[94:97], v[66:69], v[10:13] cbsz:4 blgp:4
	v_mfma_f32_16x16x128_f8f6f4 v[34:37], v[82:85], v[74:77], v[14:17] cbsz:4 blgp:4
	v_mfma_f32_16x16x128_f8f6f4 v[38:41], v[94:97], v[74:77], v[10:13] cbsz:4 blgp:4
	v_mfma_f32_16x16x128_f8f6f4 v[42:45], v[82:85], v[86:89], v[14:17] cbsz:4 blgp:4
	v_mfma_f32_16x16x128_f8f6f4 v[46:49], v[94:97], v[86:89], v[10:13] cbsz:4 blgp:4
	v_mfma_f32_16x16x128_f8f6f4 v[18:21], v[102:105], v[62:65], v[18:21] cbsz:4 blgp:4
	v_mfma_f32_16x16x128_f8f6f4 v[22:25], v[110:113], v[62:65], v[22:25] cbsz:4 blgp:4
	v_mfma_f32_16x16x128_f8f6f4 v[26:29], v[102:105], v[70:73], v[26:29] cbsz:4 blgp:4
	v_mfma_f32_16x16x128_f8f6f4 v[30:33], v[110:113], v[70:73], v[30:33] cbsz:4 blgp:4
	v_mfma_f32_16x16x128_f8f6f4 v[34:37], v[102:105], v[78:81], v[34:37] cbsz:4 blgp:4
	v_mfma_f32_16x16x128_f8f6f4 v[38:41], v[110:113], v[78:81], v[38:41] cbsz:4 blgp:4
	v_mfma_f32_16x16x128_f8f6f4 v[42:45], v[102:105], v[90:93], v[42:45] cbsz:4 blgp:4
	v_mfma_f32_16x16x128_f8f6f4 v[46:49], v[110:113], v[90:93], v[46:49] cbsz:4 blgp:4
	s_setprio 0
	s_barrier
	ds_read_b128 v[142:145], v169 offset:16384
	ds_read_b128 v[146:149], v169 offset:18432
	ds_read_b128 v[150:153], v178 offset:16384
	ds_read_b128 v[154:157], v178 offset:18432
	s_mov_b32 m0, s54
	s_nop 0
	global_load_lds_dwordx4 v164, s[46:47]
	s_mov_b32 m0, s55
	s_nop 0
	global_load_lds_dwordx4 v168, s[46:47]
	s_barrier
	s_waitcnt lgkmcnt(0)
	s_setprio 1
	v_mfma_f32_16x16x128_f8f6f4 v[50:53], v[142:145], v[58:61], v[6:9] cbsz:4 blgp:4
	v_mfma_f32_16x16x128_f8f6f4 v[54:57], v[146:149], v[58:61], v[2:5] cbsz:4 blgp:4
	v_mfma_f32_16x16x128_f8f6f4 v[50:53], v[150:153], v[62:65], v[50:53] cbsz:4 blgp:4
	v_mfma_f32_16x16x128_f8f6f4 v[54:57], v[154:157], v[62:65], v[54:57] cbsz:4 blgp:4
	v_mfma_f32_16x16x128_f8f6f4 v[58:61], v[142:145], v[66:69], v[6:9] cbsz:4 blgp:4
	v_mfma_f32_16x16x128_f8f6f4 v[62:65], v[146:149], v[66:69], v[2:5] cbsz:4 blgp:4
	v_mfma_f32_16x16x128_f8f6f4 v[58:61], v[150:153], v[70:73], v[58:61] cbsz:4 blgp:4
	v_mfma_f32_16x16x128_f8f6f4 v[62:65], v[154:157], v[70:73], v[62:65] cbsz:4 blgp:4
	v_mfma_f32_16x16x128_f8f6f4 v[66:69], v[142:145], v[74:77], v[6:9] cbsz:4 blgp:4
	v_mfma_f32_16x16x128_f8f6f4 v[70:73], v[146:149], v[74:77], v[2:5] cbsz:4 blgp:4
	v_mfma_f32_16x16x128_f8f6f4 v[66:69], v[150:153], v[78:81], v[66:69] cbsz:4 blgp:4
	v_mfma_f32_16x16x128_f8f6f4 v[70:73], v[154:157], v[78:81], v[70:73] cbsz:4 blgp:4
	v_mfma_f32_16x16x128_f8f6f4 v[74:77], v[142:145], v[86:89], v[6:9] cbsz:4 blgp:4
	v_mfma_f32_16x16x128_f8f6f4 v[78:81], v[146:149], v[86:89], v[2:5] cbsz:4 blgp:4
	v_mfma_f32_16x16x128_f8f6f4 v[74:77], v[150:153], v[90:93], v[74:77] cbsz:4 blgp:4
	v_mfma_f32_16x16x128_f8f6f4 v[78:81], v[154:157], v[90:93], v[78:81] cbsz:4 blgp:4
	s_setprio 0
	s_barrier
	ds_read_b128 v[114:117], v179 offset:16384
	ds_read_b128 v[122:125], v179 offset:18432
	ds_read_b128 v[130:133], v180 offset:16384
	ds_read_b128 v[134:137], v180 offset:18432
	ds_read_b128 v[158:161], v179 offset:20480
	ds_read_b128 v[182:185], v179 offset:22528
	ds_read_b128 v[186:189], v180 offset:20480
	ds_read_b128 v[190:193], v180 offset:22528
	s_mov_b32 m0, s53
	s_nop 0
	global_load_lds_dwordx4 v162, s[44:45]
	s_mov_b32 m0, s56
	s_nop 0
	global_load_lds_dwordx4 v166, s[44:45]
	s_barrier
	s_waitcnt lgkmcnt(0)
	s_setprio 1
	v_mfma_f32_16x16x128_f8f6f4 v[86:89], v[82:85], v[114:117], v[14:17] cbsz:4 blgp:4
	v_mfma_f32_16x16x128_f8f6f4 v[90:93], v[94:97], v[114:117], v[10:13] cbsz:4 blgp:4
	v_mfma_f32_16x16x128_f8f6f4 v[98:101], v[82:85], v[122:125], v[14:17] cbsz:4 blgp:4
	v_mfma_f32_16x16x128_f8f6f4 v[106:109], v[94:97], v[122:125], v[10:13] cbsz:4 blgp:4
	v_mfma_f32_16x16x128_f8f6f4 v[118:121], v[82:85], v[158:161], v[14:17] cbsz:4 blgp:4
	v_mfma_f32_16x16x128_f8f6f4 v[126:129], v[94:97], v[158:161], v[10:13] cbsz:4 blgp:4
	v_mfma_f32_16x16x128_f8f6f4 v[138:141], v[82:85], v[182:185], v[14:17] cbsz:4 blgp:4
	v_mfma_f32_16x16x128_f8f6f4 v[82:85], v[94:97], v[182:185], v[10:13] cbsz:4 blgp:4
	v_mfma_f32_16x16x128_f8f6f4 v[86:89], v[102:105], v[130:133], v[86:89] cbsz:4 blgp:4
	v_mfma_f32_16x16x128_f8f6f4 v[90:93], v[110:113], v[130:133], v[90:93] cbsz:4 blgp:4
	v_mfma_f32_16x16x128_f8f6f4 v[98:101], v[102:105], v[134:137], v[98:101] cbsz:4 blgp:4
	v_mfma_f32_16x16x128_f8f6f4 v[106:109], v[110:113], v[134:137], v[106:109] cbsz:4 blgp:4
	v_mfma_f32_16x16x128_f8f6f4 v[118:121], v[102:105], v[186:189], v[118:121] cbsz:4 blgp:4
	v_mfma_f32_16x16x128_f8f6f4 v[126:129], v[110:113], v[186:189], v[126:129] cbsz:4 blgp:4
	v_mfma_f32_16x16x128_f8f6f4 v[138:141], v[102:105], v[190:193], v[138:141] cbsz:4 blgp:4
	v_mfma_f32_16x16x128_f8f6f4 v[82:85], v[110:113], v[190:193], v[82:85] cbsz:4 blgp:4
	s_setprio 0
	s_barrier
	s_add_u32 s46, s46, s22
	s_addc_u32 s47, s47, s23
	s_mov_b32 m0, s57
	s_nop 0
	global_load_lds_dwordx4 v164, s[46:47]
	s_mov_b32 m0, s58
	s_nop 0
	global_load_lds_dwordx4 v168, s[46:47]
	s_waitcnt vmcnt(6)
	s_barrier
	s_setprio 1
	v_mfma_f32_16x16x128_f8f6f4 v[94:97], v[142:145], v[114:117], v[6:9] cbsz:4 blgp:4
	v_mfma_f32_16x16x128_f8f6f4 v[102:105], v[146:149], v[114:117], v[2:5] cbsz:4 blgp:4
	v_mfma_f32_16x16x128_f8f6f4 v[110:113], v[142:145], v[122:125], v[6:9] cbsz:4 blgp:4
	v_mfma_f32_16x16x128_f8f6f4 v[114:117], v[146:149], v[122:125], v[2:5] cbsz:4 blgp:4
	v_mfma_f32_16x16x128_f8f6f4 v[94:97], v[150:153], v[130:133], v[94:97] cbsz:4 blgp:4
	v_mfma_f32_16x16x128_f8f6f4 v[102:105], v[154:157], v[130:133], v[102:105] cbsz:4 blgp:4
	v_mfma_f32_16x16x128_f8f6f4 v[110:113], v[150:153], v[134:137], v[110:113] cbsz:4 blgp:4
	v_mfma_f32_16x16x128_f8f6f4 v[114:117], v[154:157], v[134:137], v[114:117] cbsz:4 blgp:4
	v_mfma_f32_16x16x128_f8f6f4 v[122:125], v[142:145], v[158:161], v[6:9] cbsz:4 blgp:4
	v_mfma_f32_16x16x128_f8f6f4 v[130:133], v[146:149], v[158:161], v[2:5] cbsz:4 blgp:4
	v_mfma_f32_16x16x128_f8f6f4 v[134:137], v[142:145], v[182:185], v[6:9] cbsz:4 blgp:4
	v_mfma_f32_16x16x128_f8f6f4 v[142:145], v[146:149], v[182:185], v[2:5] cbsz:4 blgp:4
	v_mfma_f32_16x16x128_f8f6f4 v[122:125], v[150:153], v[186:189], v[122:125] cbsz:4 blgp:4
	v_mfma_f32_16x16x128_f8f6f4 v[130:133], v[154:157], v[186:189], v[130:133] cbsz:4 blgp:4
	v_mfma_f32_16x16x128_f8f6f4 v[134:137], v[150:153], v[190:193], v[134:137] cbsz:4 blgp:4
	v_mfma_f32_16x16x128_f8f6f4 v[142:145], v[154:157], v[190:193], v[142:145] cbsz:4 blgp:4
	s_setprio 0
	s_barrier
	ds_read_b128 v[146:149], v169 offset:32768
	ds_read_b128 v[150:153], v169 offset:34816
	ds_read_b128 v[154:157], v178 offset:32768
	ds_read_b128 v[158:161], v178 offset:34816
	ds_read_b128 v[182:185], v179 offset:32768
	ds_read_b128 v[186:189], v179 offset:34816
	ds_read_b128 v[190:193], v180 offset:32768
	ds_read_b128 v[194:197], v180 offset:34816
	ds_read_b128 v[198:201], v179 offset:36864
	ds_read_b128 v[202:205], v179 offset:38912
	ds_read_b128 v[206:209], v180 offset:36864
	ds_read_b128 v[210:213], v180 offset:38912
	s_add_u32 s44, s44, s20
	s_addc_u32 s45, s45, s21
	s_mov_b32 m0, s59
	s_nop 0
	global_load_lds_dwordx4 v162, s[44:45]
	s_mov_b32 m0, s60
	s_nop 0
	global_load_lds_dwordx4 v166, s[44:45]
	s_waitcnt lgkmcnt(8)
	s_barrier
	s_waitcnt lgkmcnt(0)
	s_setprio 1
	v_mfma_f32_16x16x128_f8f6f4 v[18:21], v[146:149], v[182:185], v[18:21] cbsz:4 blgp:4
	v_mfma_f32_16x16x128_f8f6f4 v[22:25], v[150:153], v[182:185], v[22:25] cbsz:4 blgp:4
	v_mfma_f32_16x16x128_f8f6f4 v[26:29], v[146:149], v[186:189], v[26:29] cbsz:4 blgp:4
	v_mfma_f32_16x16x128_f8f6f4 v[30:33], v[150:153], v[186:189], v[30:33] cbsz:4 blgp:4
	v_mfma_f32_16x16x128_f8f6f4 v[34:37], v[146:149], v[198:201], v[34:37] cbsz:4 blgp:4
	v_mfma_f32_16x16x128_f8f6f4 v[38:41], v[150:153], v[198:201], v[38:41] cbsz:4 blgp:4
	v_mfma_f32_16x16x128_f8f6f4 v[42:45], v[146:149], v[202:205], v[42:45] cbsz:4 blgp:4
	v_mfma_f32_16x16x128_f8f6f4 v[46:49], v[150:153], v[202:205], v[46:49] cbsz:4 blgp:4
	v_mfma_f32_16x16x128_f8f6f4 v[18:21], v[154:157], v[190:193], v[18:21] cbsz:4 blgp:4
	v_mfma_f32_16x16x128_f8f6f4 v[22:25], v[158:161], v[190:193], v[22:25] cbsz:4 blgp:4
	v_mfma_f32_16x16x128_f8f6f4 v[26:29], v[154:157], v[194:197], v[26:29] cbsz:4 blgp:4
	v_mfma_f32_16x16x128_f8f6f4 v[30:33], v[158:161], v[194:197], v[30:33] cbsz:4 blgp:4
	v_mfma_f32_16x16x128_f8f6f4 v[34:37], v[154:157], v[206:209], v[34:37] cbsz:4 blgp:4
	v_mfma_f32_16x16x128_f8f6f4 v[38:41], v[158:161], v[206:209], v[38:41] cbsz:4 blgp:4
	v_mfma_f32_16x16x128_f8f6f4 v[42:45], v[154:157], v[210:213], v[42:45] cbsz:4 blgp:4
	v_mfma_f32_16x16x128_f8f6f4 v[46:49], v[158:161], v[210:213], v[46:49] cbsz:4 blgp:4
	s_setprio 0
	s_barrier
	ds_read_b128 v[214:217], v169 offset:49152
	ds_read_b128 v[218:221], v169 offset:51200
	ds_read_b128 v[222:225], v178 offset:49152
	ds_read_b128 v[226:229], v178 offset:51200
	s_mov_b32 m0, s62
	s_nop 0
	global_load_lds_dwordx4 v164, s[40:41]
	s_mov_b32 m0, s63
	s_nop 0
	global_load_lds_dwordx4 v168, s[40:41]
	s_barrier
	s_waitcnt lgkmcnt(0)
	s_setprio 1
	v_mfma_f32_16x16x128_f8f6f4 v[50:53], v[214:217], v[182:185], v[50:53] cbsz:4 blgp:4
	v_mfma_f32_16x16x128_f8f6f4 v[54:57], v[218:221], v[182:185], v[54:57] cbsz:4 blgp:4
	v_mfma_f32_16x16x128_f8f6f4 v[58:61], v[214:217], v[186:189], v[58:61] cbsz:4 blgp:4
	v_mfma_f32_16x16x128_f8f6f4 v[62:65], v[218:221], v[186:189], v[62:65] cbsz:4 blgp:4
	v_mfma_f32_16x16x128_f8f6f4 v[66:69], v[214:217], v[198:201], v[66:69] cbsz:4 blgp:4
	v_mfma_f32_16x16x128_f8f6f4 v[70:73], v[218:221], v[198:201], v[70:73] cbsz:4 blgp:4
	v_mfma_f32_16x16x128_f8f6f4 v[74:77], v[214:217], v[202:205], v[74:77] cbsz:4 blgp:4
	v_mfma_f32_16x16x128_f8f6f4 v[78:81], v[218:221], v[202:205], v[78:81] cbsz:4 blgp:4
	v_mfma_f32_16x16x128_f8f6f4 v[50:53], v[222:225], v[190:193], v[50:53] cbsz:4 blgp:4
	v_mfma_f32_16x16x128_f8f6f4 v[54:57], v[226:229], v[190:193], v[54:57] cbsz:4 blgp:4
	v_mfma_f32_16x16x128_f8f6f4 v[58:61], v[222:225], v[194:197], v[58:61] cbsz:4 blgp:4
	v_mfma_f32_16x16x128_f8f6f4 v[62:65], v[226:229], v[194:197], v[62:65] cbsz:4 blgp:4
	v_mfma_f32_16x16x128_f8f6f4 v[66:69], v[222:225], v[206:209], v[66:69] cbsz:4 blgp:4
	v_mfma_f32_16x16x128_f8f6f4 v[70:73], v[226:229], v[206:209], v[70:73] cbsz:4 blgp:4
	v_mfma_f32_16x16x128_f8f6f4 v[74:77], v[222:225], v[210:213], v[74:77] cbsz:4 blgp:4
	v_mfma_f32_16x16x128_f8f6f4 v[78:81], v[226:229], v[210:213], v[78:81] cbsz:4 blgp:4
	s_setprio 0
	s_barrier
	ds_read_b128 v[182:185], v179 offset:49152
	ds_read_b128 v[186:189], v179 offset:51200
	ds_read_b128 v[190:193], v180 offset:49152
	ds_read_b128 v[194:197], v180 offset:51200
	ds_read_b128 v[198:201], v179 offset:53248
	ds_read_b128 v[202:205], v179 offset:55296
	ds_read_b128 v[206:209], v180 offset:53248
	ds_read_b128 v[210:213], v180 offset:55296
	s_mov_b32 m0, s64
	s_nop 0
	global_load_lds_dwordx4 v162, s[42:43]
	s_mov_b32 m0, s65
	s_nop 0
	global_load_lds_dwordx4 v166, s[42:43]
	s_barrier
	s_waitcnt lgkmcnt(0)
	s_setprio 1
	v_mfma_f32_16x16x128_f8f6f4 v[86:89], v[146:149], v[182:185], v[86:89] cbsz:4 blgp:4
	v_mfma_f32_16x16x128_f8f6f4 v[90:93], v[150:153], v[182:185], v[90:93] cbsz:4 blgp:4
	v_mfma_f32_16x16x128_f8f6f4 v[98:101], v[146:149], v[186:189], v[98:101] cbsz:4 blgp:4
	v_mfma_f32_16x16x128_f8f6f4 v[106:109], v[150:153], v[186:189], v[106:109] cbsz:4 blgp:4
	v_mfma_f32_16x16x128_f8f6f4 v[118:121], v[146:149], v[198:201], v[118:121] cbsz:4 blgp:4
	v_mfma_f32_16x16x128_f8f6f4 v[126:129], v[150:153], v[198:201], v[126:129] cbsz:4 blgp:4
	v_mfma_f32_16x16x128_f8f6f4 v[138:141], v[146:149], v[202:205], v[138:141] cbsz:4 blgp:4
	v_mfma_f32_16x16x128_f8f6f4 v[82:85], v[150:153], v[202:205], v[82:85] cbsz:4 blgp:4
	v_mfma_f32_16x16x128_f8f6f4 v[86:89], v[154:157], v[190:193], v[86:89] cbsz:4 blgp:4
	v_mfma_f32_16x16x128_f8f6f4 v[90:93], v[158:161], v[190:193], v[90:93] cbsz:4 blgp:4
	v_mfma_f32_16x16x128_f8f6f4 v[98:101], v[154:157], v[194:197], v[98:101] cbsz:4 blgp:4
	v_mfma_f32_16x16x128_f8f6f4 v[106:109], v[158:161], v[194:197], v[106:109] cbsz:4 blgp:4
	v_mfma_f32_16x16x128_f8f6f4 v[118:121], v[154:157], v[206:209], v[118:121] cbsz:4 blgp:4
	v_mfma_f32_16x16x128_f8f6f4 v[126:129], v[158:161], v[206:209], v[126:129] cbsz:4 blgp:4
	v_mfma_f32_16x16x128_f8f6f4 v[138:141], v[154:157], v[210:213], v[138:141] cbsz:4 blgp:4
	v_mfma_f32_16x16x128_f8f6f4 v[82:85], v[158:161], v[210:213], v[82:85] cbsz:4 blgp:4
	s_setprio 0
	s_barrier
	s_add_u32 s40, s40, s22
	s_addc_u32 s41, s41, s23
	s_mov_b32 m0, s66
	s_nop 0
	global_load_lds_dwordx4 v164, s[40:41]
	s_mov_b32 m0, s67
	s_nop 0
	global_load_lds_dwordx4 v168, s[40:41]
	s_waitcnt vmcnt(6)
	s_barrier
	s_setprio 1
	v_mfma_f32_16x16x128_f8f6f4 v[94:97], v[214:217], v[182:185], v[94:97] cbsz:4 blgp:4
	v_mfma_f32_16x16x128_f8f6f4 v[102:105], v[218:221], v[182:185], v[102:105] cbsz:4 blgp:4
	v_mfma_f32_16x16x128_f8f6f4 v[110:113], v[214:217], v[186:189], v[110:113] cbsz:4 blgp:4
	v_mfma_f32_16x16x128_f8f6f4 v[114:117], v[218:221], v[186:189], v[114:117] cbsz:4 blgp:4
	v_mfma_f32_16x16x128_f8f6f4 v[122:125], v[214:217], v[198:201], v[122:125] cbsz:4 blgp:4
	v_mfma_f32_16x16x128_f8f6f4 v[130:133], v[218:221], v[198:201], v[130:133] cbsz:4 blgp:4
	v_mfma_f32_16x16x128_f8f6f4 v[134:137], v[214:217], v[202:205], v[134:137] cbsz:4 blgp:4
	v_mfma_f32_16x16x128_f8f6f4 v[142:145], v[218:221], v[202:205], v[142:145] cbsz:4 blgp:4
	v_mfma_f32_16x16x128_f8f6f4 v[94:97], v[222:225], v[190:193], v[94:97] cbsz:4 blgp:4
	v_mfma_f32_16x16x128_f8f6f4 v[102:105], v[226:229], v[190:193], v[102:105] cbsz:4 blgp:4
	v_mfma_f32_16x16x128_f8f6f4 v[110:113], v[222:225], v[194:197], v[110:113] cbsz:4 blgp:4
	v_mfma_f32_16x16x128_f8f6f4 v[114:117], v[226:229], v[194:197], v[114:117] cbsz:4 blgp:4
	v_mfma_f32_16x16x128_f8f6f4 v[122:125], v[222:225], v[206:209], v[122:125] cbsz:4 blgp:4
	v_mfma_f32_16x16x128_f8f6f4 v[130:133], v[226:229], v[206:209], v[130:133] cbsz:4 blgp:4
	v_mfma_f32_16x16x128_f8f6f4 v[134:137], v[222:225], v[210:213], v[134:137] cbsz:4 blgp:4
	v_mfma_f32_16x16x128_f8f6f4 v[142:145], v[226:229], v[210:213], v[142:145] cbsz:4 blgp:4
	s_setprio 0
	s_andn2_b64 vcc, exec, s[28:29]
	s_barrier
	s_cbranch_vccnz .LBB6_20
	s_ashr_i32 s39, s38, 31
	s_lshl_b64 s[38:39], s[38:39], 10
	s_add_u32 s38, s14, s38
	s_addc_u32 s39, s15, s39
	s_add_u32 s31, s36, 0x200
	s_addc_u32 s46, s37, 0
	s_add_u32 s47, s34, 0x200
	s_addc_u32 s81, s35, 0
	s_add_u32 s34, s82, 0x180
	s_addc_u32 s35, s83, 0
	s_mov_b32 s82, 4
	s_cmp_eq_u32 s61, s82
	s_cselect_b64 s[36:37], -1, 0
	s_cmp_lg_u32 s61, s82
	s_cbranch_scc1 .LBB6_18

.LBB6_18:
	ds_read_b128 v[146:149], v169
	ds_read_b128 v[150:153], v169 offset:2048
	ds_read_b128 v[154:157], v178
	ds_read_b128 v[158:161], v178 offset:2048
	s_and_b64 s[36:37], s[36:37], exec
	s_cselect_b32 s42, s4, s31
	s_cselect_b32 s43, s5, s46
	s_cselect_b32 s45, s7, s81
	s_cselect_b32 s44, s6, s47
	s_add_u32 s40, s42, 0x80
	s_addc_u32 s41, s43, 0
	s_add_u32 s36, s44, 0x80
	s_addc_u32 s37, s45, 0
	ds_read_b128 v[182:185], v179
	ds_read_b128 v[186:189], v179 offset:2048
	ds_read_b128 v[190:193], v180
	ds_read_b128 v[194:197], v180 offset:2048
	ds_read_b128 v[198:201], v179 offset:4096
	ds_read_b128 v[202:205], v179 offset:6144
	ds_read_b128 v[206:209], v180 offset:4096
	ds_read_b128 v[210:213], v180 offset:6144
	s_mov_b32 m0, s68
	s_nop 0
	global_load_lds_dwordx4 v162, s[34:35]
	s_mov_b32 m0, s69
	s_nop 0
	global_load_lds_dwordx4 v166, s[34:35]
	s_waitcnt lgkmcnt(8)
	s_barrier
	s_waitcnt lgkmcnt(0)
	s_setprio 1
	v_mfma_f32_16x16x128_f8f6f4 v[18:21], v[146:149], v[182:185], v[18:21] cbsz:4 blgp:4
	v_mfma_f32_16x16x128_f8f6f4 v[22:25], v[150:153], v[182:185], v[22:25] cbsz:4 blgp:4
	v_mfma_f32_16x16x128_f8f6f4 v[26:29], v[146:149], v[186:189], v[26:29] cbsz:4 blgp:4
	v_mfma_f32_16x16x128_f8f6f4 v[30:33], v[150:153], v[186:189], v[30:33] cbsz:4 blgp:4
	v_mfma_f32_16x16x128_f8f6f4 v[34:37], v[146:149], v[198:201], v[34:37] cbsz:4 blgp:4
	v_mfma_f32_16x16x128_f8f6f4 v[38:41], v[150:153], v[198:201], v[38:41] cbsz:4 blgp:4
	v_mfma_f32_16x16x128_f8f6f4 v[42:45], v[146:149], v[202:205], v[42:45] cbsz:4 blgp:4
	v_mfma_f32_16x16x128_f8f6f4 v[46:49], v[150:153], v[202:205], v[46:49] cbsz:4 blgp:4
	v_mfma_f32_16x16x128_f8f6f4 v[18:21], v[154:157], v[190:193], v[18:21] cbsz:4 blgp:4
	v_mfma_f32_16x16x128_f8f6f4 v[22:25], v[158:161], v[190:193], v[22:25] cbsz:4 blgp:4
	v_mfma_f32_16x16x128_f8f6f4 v[26:29], v[154:157], v[194:197], v[26:29] cbsz:4 blgp:4
	v_mfma_f32_16x16x128_f8f6f4 v[30:33], v[158:161], v[194:197], v[30:33] cbsz:4 blgp:4
	v_mfma_f32_16x16x128_f8f6f4 v[34:37], v[154:157], v[206:209], v[34:37] cbsz:4 blgp:4
	v_mfma_f32_16x16x128_f8f6f4 v[38:41], v[158:161], v[206:209], v[38:41] cbsz:4 blgp:4
	v_mfma_f32_16x16x128_f8f6f4 v[42:45], v[154:157], v[210:213], v[42:45] cbsz:4 blgp:4
	v_mfma_f32_16x16x128_f8f6f4 v[46:49], v[158:161], v[210:213], v[46:49] cbsz:4 blgp:4
	s_setprio 0
	s_barrier
	ds_read_b128 v[214:217], v169 offset:16384
	ds_read_b128 v[218:221], v169 offset:18432
	ds_read_b128 v[222:225], v178 offset:16384
	ds_read_b128 v[226:229], v178 offset:18432
	s_mov_b32 m0, s54
	s_nop 0
	global_load_lds_dwordx4 v164, s[44:45]
	s_mov_b32 m0, s55
	s_nop 0
	global_load_lds_dwordx4 v168, s[44:45]
	s_barrier
	s_waitcnt lgkmcnt(0)
	s_setprio 1
	v_mfma_f32_16x16x128_f8f6f4 v[50:53], v[214:217], v[182:185], v[50:53] cbsz:4 blgp:4
	v_mfma_f32_16x16x128_f8f6f4 v[54:57], v[218:221], v[182:185], v[54:57] cbsz:4 blgp:4
	v_mfma_f32_16x16x128_f8f6f4 v[58:61], v[214:217], v[186:189], v[58:61] cbsz:4 blgp:4
	v_mfma_f32_16x16x128_f8f6f4 v[62:65], v[218:221], v[186:189], v[62:65] cbsz:4 blgp:4
	v_mfma_f32_16x16x128_f8f6f4 v[66:69], v[214:217], v[198:201], v[66:69] cbsz:4 blgp:4
	v_mfma_f32_16x16x128_f8f6f4 v[70:73], v[218:221], v[198:201], v[70:73] cbsz:4 blgp:4
	v_mfma_f32_16x16x128_f8f6f4 v[74:77], v[214:217], v[202:205], v[74:77] cbsz:4 blgp:4
	v_mfma_f32_16x16x128_f8f6f4 v[78:81], v[218:221], v[202:205], v[78:81] cbsz:4 blgp:4
	v_mfma_f32_16x16x128_f8f6f4 v[50:53], v[222:225], v[190:193], v[50:53] cbsz:4 blgp:4
	v_mfma_f32_16x16x128_f8f6f4 v[54:57], v[226:229], v[190:193], v[54:57] cbsz:4 blgp:4
	v_mfma_f32_16x16x128_f8f6f4 v[58:61], v[222:225], v[194:197], v[58:61] cbsz:4 blgp:4
	v_mfma_f32_16x16x128_f8f6f4 v[62:65], v[226:229], v[194:197], v[62:65] cbsz:4 blgp:4
	v_mfma_f32_16x16x128_f8f6f4 v[66:69], v[222:225], v[206:209], v[66:69] cbsz:4 blgp:4
	v_mfma_f32_16x16x128_f8f6f4 v[70:73], v[226:229], v[206:209], v[70:73] cbsz:4 blgp:4
	v_mfma_f32_16x16x128_f8f6f4 v[74:77], v[222:225], v[210:213], v[74:77] cbsz:4 blgp:4
	v_mfma_f32_16x16x128_f8f6f4 v[78:81], v[226:229], v[210:213], v[78:81] cbsz:4 blgp:4
	s_setprio 0
	s_barrier
	ds_read_b128 v[182:185], v179 offset:16384
	ds_read_b128 v[186:189], v179 offset:18432
	ds_read_b128 v[190:193], v180 offset:16384
	ds_read_b128 v[194:197], v180 offset:18432
	ds_read_b128 v[198:201], v179 offset:20480
	ds_read_b128 v[202:205], v179 offset:22528
	ds_read_b128 v[206:209], v180 offset:20480
	ds_read_b128 v[210:213], v180 offset:22528
	s_mov_b32 m0, s53
	s_nop 0
	global_load_lds_dwordx4 v162, s[42:43]
	s_mov_b32 m0, s56
	s_nop 0
	global_load_lds_dwordx4 v166, s[42:43]
	s_barrier
	s_waitcnt lgkmcnt(0)
	s_setprio 1
	v_mfma_f32_16x16x128_f8f6f4 v[86:89], v[146:149], v[182:185], v[86:89] cbsz:4 blgp:4
	v_mfma_f32_16x16x128_f8f6f4 v[90:93], v[150:153], v[182:185], v[90:93] cbsz:4 blgp:4
	v_mfma_f32_16x16x128_f8f6f4 v[98:101], v[146:149], v[186:189], v[98:101] cbsz:4 blgp:4
	v_mfma_f32_16x16x128_f8f6f4 v[106:109], v[150:153], v[186:189], v[106:109] cbsz:4 blgp:4
	v_mfma_f32_16x16x128_f8f6f4 v[118:121], v[146:149], v[198:201], v[118:121] cbsz:4 blgp:4
	v_mfma_f32_16x16x128_f8f6f4 v[126:129], v[150:153], v[198:201], v[126:129] cbsz:4 blgp:4
	v_mfma_f32_16x16x128_f8f6f4 v[138:141], v[146:149], v[202:205], v[138:141] cbsz:4 blgp:4
	v_mfma_f32_16x16x128_f8f6f4 v[82:85], v[150:153], v[202:205], v[82:85] cbsz:4 blgp:4
	v_mfma_f32_16x16x128_f8f6f4 v[86:89], v[154:157], v[190:193], v[86:89] cbsz:4 blgp:4
	v_mfma_f32_16x16x128_f8f6f4 v[90:93], v[158:161], v[190:193], v[90:93] cbsz:4 blgp:4
	v_mfma_f32_16x16x128_f8f6f4 v[98:101], v[154:157], v[194:197], v[98:101] cbsz:4 blgp:4
	v_mfma_f32_16x16x128_f8f6f4 v[106:109], v[158:161], v[194:197], v[106:109] cbsz:4 blgp:4
	v_mfma_f32_16x16x128_f8f6f4 v[118:121], v[154:157], v[206:209], v[118:121] cbsz:4 blgp:4
	v_mfma_f32_16x16x128_f8f6f4 v[126:129], v[158:161], v[206:209], v[126:129] cbsz:4 blgp:4
	v_mfma_f32_16x16x128_f8f6f4 v[138:141], v[154:157], v[210:213], v[138:141] cbsz:4 blgp:4
	v_mfma_f32_16x16x128_f8f6f4 v[82:85], v[158:161], v[210:213], v[82:85] cbsz:4 blgp:4
	s_setprio 0
	s_barrier
	s_add_u32 s44, s44, s22
	s_addc_u32 s45, s45, s23
	s_mov_b32 m0, s57
	s_nop 0
	global_load_lds_dwordx4 v164, s[44:45]
	s_mov_b32 m0, s58
	s_nop 0
	global_load_lds_dwordx4 v168, s[44:45]
	s_waitcnt vmcnt(6)
	s_barrier
	s_setprio 1
	v_mfma_f32_16x16x128_f8f6f4 v[94:97], v[214:217], v[182:185], v[94:97] cbsz:4 blgp:4
	v_mfma_f32_16x16x128_f8f6f4 v[102:105], v[218:221], v[182:185], v[102:105] cbsz:4 blgp:4
	v_mfma_f32_16x16x128_f8f6f4 v[110:113], v[214:217], v[186:189], v[110:113] cbsz:4 blgp:4
	v_mfma_f32_16x16x128_f8f6f4 v[114:117], v[218:221], v[186:189], v[114:117] cbsz:4 blgp:4
	v_mfma_f32_16x16x128_f8f6f4 v[122:125], v[214:217], v[198:201], v[122:125] cbsz:4 blgp:4
	v_mfma_f32_16x16x128_f8f6f4 v[130:133], v[218:221], v[198:201], v[130:133] cbsz:4 blgp:4
	v_mfma_f32_16x16x128_f8f6f4 v[134:137], v[214:217], v[202:205], v[134:137] cbsz:4 blgp:4
	v_mfma_f32_16x16x128_f8f6f4 v[142:145], v[218:221], v[202:205], v[142:145] cbsz:4 blgp:4
	v_mfma_f32_16x16x128_f8f6f4 v[94:97], v[222:225], v[190:193], v[94:97] cbsz:4 blgp:4
	v_mfma_f32_16x16x128_f8f6f4 v[102:105], v[226:229], v[190:193], v[102:105] cbsz:4 blgp:4
	v_mfma_f32_16x16x128_f8f6f4 v[110:113], v[222:225], v[194:197], v[110:113] cbsz:4 blgp:4
	v_mfma_f32_16x16x128_f8f6f4 v[114:117], v[226:229], v[194:197], v[114:117] cbsz:4 blgp:4
	v_mfma_f32_16x16x128_f8f6f4 v[122:125], v[222:225], v[206:209], v[122:125] cbsz:4 blgp:4
	v_mfma_f32_16x16x128_f8f6f4 v[130:133], v[226:229], v[206:209], v[130:133] cbsz:4 blgp:4
	v_mfma_f32_16x16x128_f8f6f4 v[134:137], v[222:225], v[210:213], v[134:137] cbsz:4 blgp:4
	v_mfma_f32_16x16x128_f8f6f4 v[142:145], v[226:229], v[210:213], v[142:145] cbsz:4 blgp:4
	s_setprio 0
	s_barrier
	ds_read_b128 v[146:149], v169 offset:32768
	ds_read_b128 v[150:153], v169 offset:34816
	ds_read_b128 v[154:157], v178 offset:32768
	ds_read_b128 v[158:161], v178 offset:34816
	ds_read_b128 v[182:185], v179 offset:32768
	ds_read_b128 v[186:189], v179 offset:34816
	ds_read_b128 v[190:193], v180 offset:32768
	ds_read_b128 v[194:197], v180 offset:34816
	ds_read_b128 v[198:201], v179 offset:36864
	ds_read_b128 v[202:205], v179 offset:38912
	ds_read_b128 v[206:209], v180 offset:36864
	ds_read_b128 v[210:213], v180 offset:38912
	s_add_u32 s42, s42, s20
	s_addc_u32 s43, s43, s21
	s_mov_b32 m0, s59
	s_nop 0
	global_load_lds_dwordx4 v162, s[42:43]
	s_mov_b32 m0, s60
	s_nop 0
	global_load_lds_dwordx4 v166, s[42:43]
	s_waitcnt lgkmcnt(8)
	s_barrier
	s_waitcnt lgkmcnt(0)
	s_setprio 1
	v_mfma_f32_16x16x128_f8f6f4 v[18:21], v[146:149], v[182:185], v[18:21] cbsz:4 blgp:4
	v_mfma_f32_16x16x128_f8f6f4 v[22:25], v[150:153], v[182:185], v[22:25] cbsz:4 blgp:4
	v_mfma_f32_16x16x128_f8f6f4 v[26:29], v[146:149], v[186:189], v[26:29] cbsz:4 blgp:4
	v_mfma_f32_16x16x128_f8f6f4 v[30:33], v[150:153], v[186:189], v[30:33] cbsz:4 blgp:4
	v_mfma_f32_16x16x128_f8f6f4 v[34:37], v[146:149], v[198:201], v[34:37] cbsz:4 blgp:4
	v_mfma_f32_16x16x128_f8f6f4 v[38:41], v[150:153], v[198:201], v[38:41] cbsz:4 blgp:4
	v_mfma_f32_16x16x128_f8f6f4 v[42:45], v[146:149], v[202:205], v[42:45] cbsz:4 blgp:4
	v_mfma_f32_16x16x128_f8f6f4 v[46:49], v[150:153], v[202:205], v[46:49] cbsz:4 blgp:4
	v_mfma_f32_16x16x128_f8f6f4 v[18:21], v[154:157], v[190:193], v[18:21] cbsz:4 blgp:4
	v_mfma_f32_16x16x128_f8f6f4 v[22:25], v[158:161], v[190:193], v[22:25] cbsz:4 blgp:4
	v_mfma_f32_16x16x128_f8f6f4 v[26:29], v[154:157], v[194:197], v[26:29] cbsz:4 blgp:4
	v_mfma_f32_16x16x128_f8f6f4 v[30:33], v[158:161], v[194:197], v[30:33] cbsz:4 blgp:4
	v_mfma_f32_16x16x128_f8f6f4 v[34:37], v[154:157], v[206:209], v[34:37] cbsz:4 blgp:4
	v_mfma_f32_16x16x128_f8f6f4 v[38:41], v[158:161], v[206:209], v[38:41] cbsz:4 blgp:4
	v_mfma_f32_16x16x128_f8f6f4 v[42:45], v[154:157], v[210:213], v[42:45] cbsz:4 blgp:4
	v_mfma_f32_16x16x128_f8f6f4 v[46:49], v[158:161], v[210:213], v[46:49] cbsz:4 blgp:4
	s_setprio 0
	s_barrier
	ds_read_b128 v[214:217], v169 offset:49152
	ds_read_b128 v[218:221], v169 offset:51200
	ds_read_b128 v[222:225], v178 offset:49152
	ds_read_b128 v[226:229], v178 offset:51200
	s_mov_b32 m0, s62
	s_nop 0
	global_load_lds_dwordx4 v164, s[36:37]
	s_mov_b32 m0, s63
	s_nop 0
	global_load_lds_dwordx4 v168, s[36:37]
	s_barrier
	s_waitcnt lgkmcnt(0)
	s_setprio 1
	v_mfma_f32_16x16x128_f8f6f4 v[50:53], v[214:217], v[182:185], v[50:53] cbsz:4 blgp:4
	v_mfma_f32_16x16x128_f8f6f4 v[54:57], v[218:221], v[182:185], v[54:57] cbsz:4 blgp:4
	v_mfma_f32_16x16x128_f8f6f4 v[58:61], v[214:217], v[186:189], v[58:61] cbsz:4 blgp:4
	v_mfma_f32_16x16x128_f8f6f4 v[62:65], v[218:221], v[186:189], v[62:65] cbsz:4 blgp:4
	v_mfma_f32_16x16x128_f8f6f4 v[66:69], v[214:217], v[198:201], v[66:69] cbsz:4 blgp:4
	v_mfma_f32_16x16x128_f8f6f4 v[70:73], v[218:221], v[198:201], v[70:73] cbsz:4 blgp:4
	v_mfma_f32_16x16x128_f8f6f4 v[74:77], v[214:217], v[202:205], v[74:77] cbsz:4 blgp:4
	v_mfma_f32_16x16x128_f8f6f4 v[78:81], v[218:221], v[202:205], v[78:81] cbsz:4 blgp:4
	v_mfma_f32_16x16x128_f8f6f4 v[50:53], v[222:225], v[190:193], v[50:53] cbsz:4 blgp:4
	v_mfma_f32_16x16x128_f8f6f4 v[54:57], v[226:229], v[190:193], v[54:57] cbsz:4 blgp:4
	v_mfma_f32_16x16x128_f8f6f4 v[58:61], v[222:225], v[194:197], v[58:61] cbsz:4 blgp:4
	v_mfma_f32_16x16x128_f8f6f4 v[62:65], v[226:229], v[194:197], v[62:65] cbsz:4 blgp:4
	v_mfma_f32_16x16x128_f8f6f4 v[66:69], v[222:225], v[206:209], v[66:69] cbsz:4 blgp:4
	v_mfma_f32_16x16x128_f8f6f4 v[70:73], v[226:229], v[206:209], v[70:73] cbsz:4 blgp:4
	v_mfma_f32_16x16x128_f8f6f4 v[74:77], v[222:225], v[210:213], v[74:77] cbsz:4 blgp:4
	v_mfma_f32_16x16x128_f8f6f4 v[78:81], v[226:229], v[210:213], v[78:81] cbsz:4 blgp:4
	s_setprio 0
	s_barrier
	ds_read_b128 v[182:185], v179 offset:49152
	ds_read_b128 v[186:189], v179 offset:51200
	ds_read_b128 v[190:193], v180 offset:49152
	ds_read_b128 v[194:197], v180 offset:51200
	ds_read_b128 v[198:201], v179 offset:53248
	ds_read_b128 v[202:205], v179 offset:55296
	ds_read_b128 v[206:209], v180 offset:53248
	ds_read_b128 v[210:213], v180 offset:55296
	s_mov_b32 m0, s64
	s_nop 0
	global_load_lds_dwordx4 v162, s[40:41]
	s_mov_b32 m0, s65
	s_nop 0
	global_load_lds_dwordx4 v166, s[40:41]
	s_barrier
	s_waitcnt lgkmcnt(0)
	s_setprio 1
	v_mfma_f32_16x16x128_f8f6f4 v[86:89], v[146:149], v[182:185], v[86:89] cbsz:4 blgp:4
	v_mfma_f32_16x16x128_f8f6f4 v[90:93], v[150:153], v[182:185], v[90:93] cbsz:4 blgp:4
	v_mfma_f32_16x16x128_f8f6f4 v[98:101], v[146:149], v[186:189], v[98:101] cbsz:4 blgp:4
	v_mfma_f32_16x16x128_f8f6f4 v[106:109], v[150:153], v[186:189], v[106:109] cbsz:4 blgp:4
	v_mfma_f32_16x16x128_f8f6f4 v[118:121], v[146:149], v[198:201], v[118:121] cbsz:4 blgp:4
	v_mfma_f32_16x16x128_f8f6f4 v[126:129], v[150:153], v[198:201], v[126:129] cbsz:4 blgp:4
	v_mfma_f32_16x16x128_f8f6f4 v[138:141], v[146:149], v[202:205], v[138:141] cbsz:4 blgp:4
	v_mfma_f32_16x16x128_f8f6f4 v[82:85], v[150:153], v[202:205], v[82:85] cbsz:4 blgp:4
	v_mfma_f32_16x16x128_f8f6f4 v[86:89], v[154:157], v[190:193], v[86:89] cbsz:4 blgp:4
	v_mfma_f32_16x16x128_f8f6f4 v[90:93], v[158:161], v[190:193], v[90:93] cbsz:4 blgp:4
	v_mfma_f32_16x16x128_f8f6f4 v[98:101], v[154:157], v[194:197], v[98:101] cbsz:4 blgp:4
	v_mfma_f32_16x16x128_f8f6f4 v[106:109], v[158:161], v[194:197], v[106:109] cbsz:4 blgp:4
	v_mfma_f32_16x16x128_f8f6f4 v[118:121], v[154:157], v[206:209], v[118:121] cbsz:4 blgp:4
	v_mfma_f32_16x16x128_f8f6f4 v[126:129], v[158:161], v[206:209], v[126:129] cbsz:4 blgp:4
	v_mfma_f32_16x16x128_f8f6f4 v[138:141], v[154:157], v[210:213], v[138:141] cbsz:4 blgp:4
	v_mfma_f32_16x16x128_f8f6f4 v[82:85], v[158:161], v[210:213], v[82:85] cbsz:4 blgp:4
	s_setprio 0
	s_barrier
	s_add_u32 s36, s36, s22
	s_addc_u32 s37, s37, s23
	s_mov_b32 m0, s66
	s_nop 0
	global_load_lds_dwordx4 v164, s[36:37]
	s_mov_b32 m0, s67
	s_nop 0
	global_load_lds_dwordx4 v168, s[36:37]
	s_waitcnt vmcnt(6)
	s_barrier
	s_setprio 1
	v_mfma_f32_16x16x128_f8f6f4 v[94:97], v[214:217], v[182:185], v[94:97] cbsz:4 blgp:4
	v_mfma_f32_16x16x128_f8f6f4 v[102:105], v[218:221], v[182:185], v[102:105] cbsz:4 blgp:4
	v_mfma_f32_16x16x128_f8f6f4 v[110:113], v[214:217], v[186:189], v[110:113] cbsz:4 blgp:4
	v_mfma_f32_16x16x128_f8f6f4 v[114:117], v[218:221], v[186:189], v[114:117] cbsz:4 blgp:4
	v_mfma_f32_16x16x128_f8f6f4 v[122:125], v[214:217], v[198:201], v[122:125] cbsz:4 blgp:4
	v_mfma_f32_16x16x128_f8f6f4 v[130:133], v[218:221], v[198:201], v[130:133] cbsz:4 blgp:4
	v_mfma_f32_16x16x128_f8f6f4 v[134:137], v[214:217], v[202:205], v[134:137] cbsz:4 blgp:4
	v_mfma_f32_16x16x128_f8f6f4 v[142:145], v[218:221], v[202:205], v[142:145] cbsz:4 blgp:4
	v_mfma_f32_16x16x128_f8f6f4 v[94:97], v[222:225], v[190:193], v[94:97] cbsz:4 blgp:4
	v_mfma_f32_16x16x128_f8f6f4 v[102:105], v[226:229], v[190:193], v[102:105] cbsz:4 blgp:4
	v_mfma_f32_16x16x128_f8f6f4 v[110:113], v[222:225], v[194:197], v[110:113] cbsz:4 blgp:4
	v_mfma_f32_16x16x128_f8f6f4 v[114:117], v[226:229], v[194:197], v[114:117] cbsz:4 blgp:4
	v_mfma_f32_16x16x128_f8f6f4 v[122:125], v[222:225], v[206:209], v[122:125] cbsz:4 blgp:4
	v_mfma_f32_16x16x128_f8f6f4 v[130:133], v[226:229], v[206:209], v[130:133] cbsz:4 blgp:4
	v_mfma_f32_16x16x128_f8f6f4 v[134:137], v[222:225], v[210:213], v[134:137] cbsz:4 blgp:4
	v_mfma_f32_16x16x128_f8f6f4 v[142:145], v[226:229], v[210:213], v[142:145] cbsz:4 blgp:4
	s_setprio 0
	s_add_i32 s36, s82, 2
	s_add_u32 s31, s31, 0x100
	s_addc_u32 s46, s46, 0
	s_add_u32 s47, s47, 0x100
	s_addc_u32 s81, s81, 0
	s_add_u32 s34, s34, 0x100
	s_addc_u32 s35, s35, 0
	s_cmp_ge_i32 s82, s61
	s_barrier
	s_cbranch_scc1 .LBB6_20
	s_mov_b32 s82, s36
	s_cmp_eq_u32 s61, s82
	s_cselect_b64 s[36:37], -1, 0
	s_cmp_lg_u32 s61, s82
	s_cbranch_scc0 .LBB6_17
	s_branch .LBB6_18
